# route phases: router bias via an LDS table (no per-round global load + vmcnt(0)), first ten row loads of the next round issued right after the last router MFMA; stacked
# speedup vs baseline: 1.0090x; 1.0052x over previous
.LBB0_583:
	s_cmp_lt_i32 s30, 5
	s_cselect_b64 s[2:3], -1, 0
	s_add_u32 s52, s28, 0x100000
	s_addc_u32 s53, s29, 0
	s_add_u32 s90, s28, 0x110000
	s_addc_u32 s91, s29, 0
	s_add_u32 s84, s28, 0x130000
	s_addc_u32 s85, s29, 0
	s_and_b64 s[44:45], s[2:3], s[0:1]
	s_andn2_b64 vcc, exec, s[44:45]
	s_cbranch_vccnz .LBB0_607
	s_cmpk_gt_i32 s93, 0xff
	s_cbranch_scc1 .LBB0_607
	v_readlane_b32 s0, v254, 12
	v_and_b32_e32 v5, 63, v0
	v_readlane_b32 s0, v254, 0
	s_andn2_b32 s0, s0, 63
	v_lshrrev_b32_e32 v1, 4, v5
	v_readlane_b32 s1, v254, 13
	v_or_b32_e32 v2, s0, v1
	v_mov_b32_e32 v125, 0
	v_mad_i64_i32 v[2:3], s[0:1], v2, 48, 0
	v_lshlrev_b32_e32 v122, 5, v5
	v_mov_b32_e32 v123, v125
	v_readlane_b32 s6, v254, 18
	v_readlane_b32 s14, v254, 26
	v_readlane_b32 s15, v254, 27
	v_and_b32_e32 v4, 15, v0
	v_readlane_b32 s0, v254, 10
	v_lshl_add_u64 v[18:19], s[14:15], 0, v[122:123]
	v_or_b32_e32 v2, v2, v4
	v_readlane_b32 s1, v254, 11
	v_readlane_b32 s6, v254, 8
	s_movk_i32 s34, 0x1000
	v_readlane_b32 s3, v254, 15
	s_mov_b64 s[46:47], 0x1000
	s_mov_b64 s[48:49], 0x1800
	v_lshl_add_u64 v[126:127], v[2:3], 4, s[0:1]
	s_lshl_b32 s0, s6, 10
	v_add_co_u32_e32 v22, vcc, s34, v18
	v_lshl_add_u64 v[26:27], v[18:19], 0, s[46:47]
	v_lshl_add_u64 v[30:31], v[18:19], 0, s[48:49]
	v_mul_u32_u24_e32 v2, 0x2010, v4
	s_add_i32 s0, s0, 0
	v_and_b32_e32 v3, 48, v5
	s_add_i32 s3, 0, 0x20100
	v_addc_co_u32_e32 v23, vcc, 0, v19, vcc
	v_lshl_add_u64 v[128:129], s[50:51], 0, v[122:123]
	v_lshlrev_b32_e32 v124, 4, v5
	v_add3_u32 v123, s0, v2, v3
	s_waitcnt vmcnt(0)
	v_lshl_add_u32 v34, v4, 2, s3
	v_cmp_eq_u32_e64 s[0:1], 0, v5
	global_load_dwordx4 v[2:5], v122, s[14:15] offset:16
	global_load_dwordx4 v[6:9], v122, s[14:15]
	global_load_dwordx4 v[10:13], v122, s[14:15] offset:2064
	global_load_dwordx4 v[14:17], v122, s[14:15] offset:2048
	global_load_dwordx4 v[18:21], v[22:23], off
	s_nop 0
	global_load_dwordx4 v[22:25], v[22:23], off offset:2048
	s_nop 0
	global_load_dwordx4 v[26:29], v[26:27], off offset:16
	s_nop 0
	global_load_dwordx4 v[30:33], v[30:31], off offset:16
	v_readlane_b32 s2, v254, 14
	v_readlane_b32 s4, v254, 16
	s_lshl_b32 s2, s6, 1
	s_mul_i32 s4, s6, 0x4020
	s_or_b32 s27, s2, 1
	v_readlane_b32 s5, v254, 17
	s_add_i32 s26, s4, 0
	s_mul_i32 s4, s27, 0x2010
	s_add_i32 s33, s4, 0
	s_mov_b64 s[4:5], 0x1900
	v_lshl_add_u64 v[134:135], v[126:127], 0, s[4:5]
	s_mov_b64 s[4:5], 0x1a00
	v_lshl_add_u64 v[136:137], v[126:127], 0, s[4:5]
	s_mov_b64 s[4:5], 0x2400
	v_lshl_add_u64 v[138:139], v[126:127], 0, s[4:5]
	s_mov_b64 s[4:5], 0x2500
	v_lshl_add_u64 v[140:141], v[126:127], 0, s[4:5]
	s_mov_b64 s[4:5], 0x2600
	v_lshl_add_u64 v[142:143], v[126:127], 0, s[4:5]
	s_mov_b64 s[4:5], 0x3000
	v_lshl_add_u64 v[144:145], v[126:127], 0, s[4:5]
	s_mov_b64 s[4:5], 0x3100
	v_lshl_add_u64 v[146:147], v[126:127], 0, s[4:5]
	s_mov_b64 s[4:5], 0x3200
	v_lshl_add_u64 v[148:149], v[126:127], 0, s[4:5]
	s_mov_b64 s[4:5], 0x3c00
	v_lshl_add_u64 v[150:151], v[126:127], 0, s[4:5]
	s_mov_b64 s[4:5], 0x3d00
	v_lshl_add_u64 v[152:153], v[126:127], 0, s[4:5]
	s_mov_b64 s[4:5], 0x3e00
	v_lshl_add_u64 v[154:155], v[126:127], 0, s[4:5]
	s_mov_b64 s[4:5], 0x4800
	v_lshl_add_u64 v[156:157], v[126:127], 0, s[4:5]
	s_mov_b64 s[4:5], 0x4900
	v_lshl_add_u64 v[158:159], v[126:127], 0, s[4:5]
	s_mov_b64 s[4:5], 0x4a00
	v_lshl_add_u64 v[160:161], v[126:127], 0, s[4:5]
	s_mov_b64 s[4:5], 0x5400
	v_lshl_add_u64 v[162:163], v[126:127], 0, s[4:5]
	s_mov_b64 s[4:5], 0x5500
	v_lshl_add_u64 v[164:165], v[126:127], 0, s[4:5]
	s_mov_b64 s[4:5], 0x5600
	v_lshl_add_u64 v[166:167], v[126:127], 0, s[4:5]
	s_mov_b64 s[4:5], 0x6000
	v_lshl_add_u64 v[168:169], v[126:127], 0, s[4:5]
	s_mov_b64 s[4:5], 0x6100
	v_lshl_add_u64 v[170:171], v[126:127], 0, s[4:5]
	s_mov_b64 s[4:5], 0x6200
	v_lshl_add_u64 v[172:173], v[126:127], 0, s[4:5]
	s_mov_b64 s[4:5], 0x6c00
	v_lshl_add_u64 v[174:175], v[126:127], 0, s[4:5]
	s_mov_b64 s[4:5], 0x6d00
	v_lshl_add_u64 v[176:177], v[126:127], 0, s[4:5]
	s_mov_b64 s[4:5], 0x6e00
	v_lshl_add_u64 v[178:179], v[126:127], 0, s[4:5]
	s_mov_b64 s[4:5], 0x7800
	v_lshl_add_u64 v[180:181], v[126:127], 0, s[4:5]
	s_mov_b64 s[4:5], 0x7900
	v_lshl_add_u64 v[182:183], v[126:127], 0, s[4:5]
	s_mov_b64 s[4:5], 0x7a00
	v_lshl_add_u64 v[184:185], v[126:127], 0, s[4:5]
	s_mov_b64 s[4:5], 0x8400
	v_lshl_add_u64 v[186:187], v[126:127], 0, s[4:5]
	s_mov_b64 s[4:5], 0x8500
	v_lshl_add_u64 v[188:189], v[126:127], 0, s[4:5]
	s_mov_b64 s[4:5], 0x8600
	v_lshl_add_u64 v[190:191], v[126:127], 0, s[4:5]
	s_mov_b64 s[4:5], 0x9000
	v_lshl_add_u64 v[192:193], v[126:127], 0, s[4:5]
	s_mov_b64 s[4:5], 0x9100
	v_lshl_add_u64 v[194:195], v[126:127], 0, s[4:5]
	s_mov_b64 s[4:5], 0x9200
	v_lshl_add_u64 v[196:197], v[126:127], 0, s[4:5]
	s_mov_b64 s[4:5], 0x9c00
	v_lshl_add_u64 v[198:199], v[126:127], 0, s[4:5]
	s_mov_b64 s[4:5], 0x9d00
	v_lshl_add_u64 v[200:201], v[126:127], 0, s[4:5]
	s_mov_b64 s[4:5], 0x9e00
	v_lshl_add_u64 v[202:203], v[126:127], 0, s[4:5]
	s_mov_b64 s[4:5], 0xa800
	v_lshl_add_u64 v[204:205], v[126:127], 0, s[4:5]
	s_mov_b64 s[4:5], 0xa900
	v_lshl_add_u64 v[206:207], v[126:127], 0, s[4:5]
	s_mov_b64 s[4:5], 0xaa00
	v_lshl_add_u64 v[208:209], v[126:127], 0, s[4:5]
	s_mov_b64 s[4:5], 0xb400
	v_lshl_add_u64 v[210:211], v[126:127], 0, s[4:5]
	s_mov_b64 s[4:5], 0xb500
	v_lshlrev_b32_e32 v1, 2, v1
	v_lshl_add_u64 v[212:213], v[126:127], 0, s[4:5]
	s_mov_b64 s[4:5], 0xb600
	v_lshl_or_b32 v1, s6, 4, v1
	v_lshl_add_u64 v[214:215], v[126:127], 0, s[4:5]
	s_movk_i32 s4, 0xc0
	v_mul_lo_u32 v1, v1, s4
	s_mul_i32 s4, s6, 0x140
	s_add_i32 s35, 0, 0x26100
	s_add_i32 s40, s35, s4
	s_mul_i32 s4, s27, 0xa0
	v_readlane_b32 s10, v254, 22
	v_readlane_b32 s11, v254, 23
	s_add_i32 s41, s35, s4
	s_movk_i32 s4, 0x240
	s_add_i32 s6, 0, 0x26b00
	v_mbcnt_lo_u32_b32 v35, -1, 0
	v_lshl_add_u64 v[130:131], s[36:37], 0, v[124:125]
	v_lshl_add_u64 v[132:133], v[126:127], 0, s[48:49]
	v_cmp_gt_u32_e64 s[10:11], 32, v0
	v_cmp_gt_u32_e64 s[4:5], s4, v0
	v_lshl_add_u32 v219, v0, 2, s6
	v_mbcnt_hi_u32_b32 v220, -1, v35
	v_mov_b32_e32 v221, 0x358637bd
	s_mov_b32 s56, 0xf800000
	v_mov_b32_e32 v222, 0x260
	v_add_u32_e32 v223, v34, v1
	s_mov_b32 s57, 0xe38f
	s_mov_b32 s62, 0xff61b1e6
	v_mov_b32_e32 v224, 0xff61b1e6
	v_readlane_b32 s7, v254, 19
	v_readlane_b32 s8, v254, 20
	v_readlane_b32 s9, v254, 21
	v_readlane_b32 s12, v254, 24
	v_readlane_b32 s13, v254, 25
	v_mov_b32_e32 v40, v0
	v_mov_b32_e32 v45, 0
	v_mul_u32_u24_sdwa v41, v40, s57 dst_sel:DWORD dst_unused:UNUSED_PAD src0_sel:WORD_0 src1_sel:DWORD
	v_lshrrev_b32_e32 v41, 21, v41
	v_mul_lo_u16_e32 v42, 36, v41
	v_sub_u16_e32 v42, v40, v42
	v_lshlrev_b32_e32 v44, 2, v42
	v_lshl_add_u64 v[38:39], s[42:43], 0, v[44:45]
	v_lshl_add_u64 v[36:37], s[38:39], 0, v[44:45]
	v_lshl_add_u64 v[38:39], v[38:39], 0, -16
	v_cmp_gt_u16_e32 vcc, 4, v42
	s_nop 1
	v_cndmask_b32_e32 v37, v39, v37, vcc
	v_cndmask_b32_e32 v36, v38, v36, vcc
	global_load_dword v42, v[36:37], off
	v_lshlrev_b32_e32 v43, 2, v40
	v_add_u32_e32 v43, 0x26c00, v43
	s_waitcnt vmcnt(0)
	ds_write_b32 v43, v42
	v_add_u32_e32 v40, 0x200, v40
	v_cmp_gt_u32_e32 vcc, 0x240, v40
	s_and_saveexec_b64 s[14:15], vcc
	v_mul_u32_u24_sdwa v41, v40, s57 dst_sel:DWORD dst_unused:UNUSED_PAD src0_sel:WORD_0 src1_sel:DWORD
	v_lshrrev_b32_e32 v41, 21, v41
	v_mul_lo_u16_e32 v42, 36, v41
	v_sub_u16_e32 v42, v40, v42
	v_lshlrev_b32_e32 v44, 2, v42
	v_lshl_add_u64 v[38:39], s[42:43], 0, v[44:45]
	v_lshl_add_u64 v[36:37], s[38:39], 0, v[44:45]
	v_lshl_add_u64 v[38:39], v[38:39], 0, -16
	v_cmp_gt_u16_e32 vcc, 4, v42
	s_nop 1
	v_cndmask_b32_e32 v37, v39, v37, vcc
	v_cndmask_b32_e32 v36, v38, v36, vcc
	global_load_dword v42, v[36:37], off
	v_lshlrev_b32_e32 v43, 2, v40
	v_add_u32_e32 v43, 0x26c00, v43
	s_waitcnt vmcnt(0)
	ds_write_b32 v43, v42
	s_or_b64 exec, exec, s[14:15]
	s_branch .LBB0_587

.LBB0_587:
	s_and_saveexec_b64 s[6:7], s[10:11]
	ds_write_b32 v219, v125
	s_or_b64 exec, exec, s[6:7]
	s_lshl_b32 s66, s93, 6
	s_add_i32 s67, s66, s2
	s_mov_b32 s68, 0
	s_waitcnt lgkmcnt(0)
	s_barrier
	s_mov_b32 s82, 0
	s_lshl_b32 s82, s82, 4
	s_add_i32 s82, s67, s82
	s_ashr_i32 s83, s82, 31
	s_lshl_b64 s[82:83], s[82:83], 13
	v_lshl_add_u64 v[98:99], v[128:129], 0, s[82:83]
	s_add_u32 s82, s82, 0x1000
	s_addc_u32 s83, s83, 0
	global_load_dwordx4 v[118:121], v[98:99], off
	global_load_dwordx4 v[114:117], v[98:99], off offset:16
	global_load_dwordx4 v[110:113], v[98:99], off offset:2048
	global_load_dwordx4 v[106:109], v[98:99], off offset:2064
	v_lshl_add_u64 v[100:101], v[128:129], 0, s[82:83]
	s_add_u32 s82, s82, 0x1000
	s_addc_u32 s83, s83, 0
	global_load_dwordx4 v[58:61], v[100:101], off offset:2064
	global_load_dwordx4 v[90:93], v[100:101], off
	global_load_dwordx4 v[66:69], v[100:101], off offset:16
	global_load_dwordx4 v[62:65], v[100:101], off offset:2048
	v_lshl_add_u64 v[98:99], v[128:129], 0, s[82:83]
	s_nop 0
	global_load_dwordx4 v[54:57], v[98:99], off
	global_load_dwordx4 v[50:53], v[98:99], off offset:16
	s_branch .LBB0_592

.LBB0_592:
	s_lshl_b32 s8, s68, 4
	s_add_i32 s6, s67, s8
	s_ashr_i32 s7, s6, 31
	s_lshl_b64 s[12:13], s[6:7], 13
	v_lshl_add_u64 v[34:35], v[128:129], 0, s[12:13]
	v_lshl_add_u64 v[36:37], v[34:35], 0, s[48:49]
	v_add_co_u32_e32 v36, vcc, 0x1000, v34
	v_and_b32_e32 v1, 64, v220
	s_nop 0
	v_addc_co_u32_e32 v37, vcc, 0, v35, vcc
	v_lshl_add_u64 v[34:35], v[34:35], 0, s[46:47]
	v_xor_b32_e32 v34, 1, v220
	v_add_u32_e32 v1, 64, v1
	s_or_b32 s6, s6, 1
	v_cmp_lt_i32_e32 vcc, v34, v1
	s_ashr_i32 s7, s6, 31
	s_lshl_b64 s[6:7], s[6:7], 13
	v_cndmask_b32_e32 v34, v220, v34, vcc
	v_lshlrev_b32_e32 v218, 2, v34
	v_lshl_add_u64 v[34:35], v[128:129], 0, s[6:7]
	global_load_dwordx4 v[42:45], v[34:35], off offset:2064
	global_load_dwordx4 v[46:49], v[34:35], off offset:2048
	v_add_co_u32_e32 v70, vcc, s34, v34
	v_lshl_add_u64 v[36:37], v[34:35], 0, s[46:47]
	s_nop 0
	v_addc_co_u32_e32 v71, vcc, 0, v35, vcc
	v_lshl_add_u64 v[72:73], v[34:35], 0, s[48:49]
	global_load_dwordx4 v[38:41], v[70:71], off
	s_nop 0
	global_load_dwordx4 v[34:37], v[36:37], off offset:16
	s_add_i32 s8, s8, s66
	s_add_i32 s54, s8, s2
	s_ashr_i32 s55, s54, 31
	s_add_i32 s58, s8, s27
	s_ashr_i32 s59, s58, 31
	s_waitcnt vmcnt(13)
	v_mov_b32_e32 v76, v119
	s_waitcnt vmcnt(12)
	v_mov_b32_e32 v77, v115
	v_mov_b32_e32 v80, v121
	v_mov_b32_e32 v81, v117
	v_mov_b32_e32 v74, v118
	v_mov_b32_e32 v75, v114
	v_mov_b32_e32 v78, v120
	v_mov_b32_e32 v79, v116
	s_waitcnt vmcnt(11)
	v_pk_mul_f32 v[82:83], v[112:113], v[112:113]
	v_pk_mul_f32 v[84:85], v[110:111], v[110:111]
	v_pk_mul_f32 v[76:77], v[76:77], v[76:77]
	v_pk_mul_f32 v[80:81], v[80:81], v[80:81]
	v_pk_mov_b32 v[94:95], v[84:85], v[82:83] op_sel:[1,0]
	v_mov_b32_e32 v85, v83
	v_pk_fma_f32 v[74:75], v[74:75], v[74:75], v[76:77]
	v_pk_fma_f32 v[76:77], v[78:79], v[78:79], v[80:81]
	s_waitcnt vmcnt(10)
	v_mul_f32_e32 v86, v107, v107
	v_mul_f32_e32 v88, v109, v109
	v_pk_add_f32 v[78:79], v[94:95], v[84:85]
	v_pk_add_f32 v[74:75], v[74:75], v[76:77]
	v_pk_fma_f32 v[82:83], v[106:107], v[106:107], v[86:87] op_sel_hi:[1,1,0]
	v_pk_fma_f32 v[86:87], v[108:109], v[108:109], v[88:89] op_sel_hi:[1,1,0]
	s_waitcnt vmcnt(8)
	v_mul_f32_e32 v95, v90, v90
	v_mul_f32_e32 v100, v91, v91
	v_pk_add_f32 v[76:77], v[78:79], v[78:79] op_sel:[0,1] op_sel_hi:[1,0]
	v_pk_add_f32 v[74:75], v[74:75], v[74:75] op_sel:[0,1] op_sel_hi:[1,0]
	v_mul_f32_e32 v83, v92, v92
	v_mul_f32_e32 v87, v93, v93
	s_waitcnt vmcnt(7)
	v_pk_mul_f32 v[80:81], v[68:69], v[68:69]
	v_pk_mul_f32 v[84:85], v[66:67], v[66:67]
	v_mov_b32_e32 v77, v100
	v_mov_b32_e32 v75, v95
	v_pk_mov_b32 v[78:79], v[84:85], v[80:81] op_sel:[1,0]
	v_mov_b32_e32 v85, v81
	v_pk_add_f32 v[82:83], v[82:83], v[86:87]
	v_pk_add_f32 v[74:75], v[74:75], v[76:77]
	s_waitcnt vmcnt(6)
	v_mul_f32_e32 v88, v63, v63
	v_mul_f32_e32 v94, v65, v65
	v_pk_add_f32 v[78:79], v[78:79], v[84:85]
	v_pk_add_f32 v[74:75], v[74:75], v[82:83]
	v_mul_f32_e32 v96, v58, v58
	v_mul_f32_e32 v97, v59, v59
	v_mul_f32_e32 v98, v60, v60
	v_mul_f32_e32 v99, v61, v61
	v_pk_fma_f32 v[80:81], v[62:63], v[62:63], v[88:89] op_sel_hi:[1,1,0]
	v_pk_fma_f32 v[88:89], v[64:65], v[64:65], v[94:95] op_sel_hi:[1,1,0]
	v_pk_add_f32 v[78:79], v[78:79], v[78:79] op_sel:[0,1] op_sel_hi:[1,0]
	v_pk_add_f32 v[74:75], v[74:75], v[74:75] op_sel:[0,1] op_sel_hi:[1,0]
	v_mov_b32_e32 v81, v98
	v_mov_b32_e32 v79, v97
	v_mov_b32_e32 v75, v96
	v_mov_b32_e32 v89, v99
	v_pk_add_f32 v[74:75], v[74:75], v[78:79]
	v_pk_add_f32 v[76:77], v[80:81], v[88:89]
	global_load_dwordx4 v[102:105], v[70:71], off offset:2048
	global_load_dwordx4 v[98:101], v[72:73], off offset:16
	global_load_dwordx4 v[82:85], v[126:127], off
	global_load_dwordx4 v[86:89], v[126:127], off offset:256
	v_pk_add_f32 v[74:75], v[74:75], v[76:77]
	v_xor_b32_e32 v76, 2, v220
	v_add_f32_e32 v74, v74, v75
	ds_bpermute_b32 v75, v218, v74
	v_cmp_lt_i32_e32 vcc, v76, v1
	s_waitcnt lgkmcnt(0)
	v_add_f32_e32 v74, v74, v75
	v_cndmask_b32_e32 v76, v220, v76, vcc
	v_lshlrev_b32_e32 v225, 2, v76
	ds_bpermute_b32 v75, v225, v74
	v_xor_b32_e32 v76, 4, v220
	v_cmp_lt_i32_e32 vcc, v76, v1
	s_waitcnt lgkmcnt(0)
	v_add_f32_e32 v74, v74, v75
	v_cndmask_b32_e32 v76, v220, v76, vcc
	v_lshlrev_b32_e32 v230, 2, v76
	ds_bpermute_b32 v75, v230, v74
	v_xor_b32_e32 v76, 8, v220
	v_cmp_lt_i32_e32 vcc, v76, v1
	s_waitcnt lgkmcnt(0)
	v_add_f32_e32 v74, v74, v75
	v_cndmask_b32_e32 v76, v220, v76, vcc
	v_lshlrev_b32_e32 v231, 2, v76
	ds_bpermute_b32 v75, v231, v74
	v_xor_b32_e32 v76, 16, v220
	v_cmp_lt_i32_e32 vcc, v76, v1
	s_waitcnt lgkmcnt(0)
	v_add_f32_e32 v74, v74, v75
	v_cndmask_b32_e32 v76, v220, v76, vcc
	v_lshlrev_b32_e32 v232, 2, v76
	ds_bpermute_b32 v75, v232, v74
	v_xor_b32_e32 v76, 32, v220
	v_cmp_lt_i32_e32 vcc, v76, v1
	s_waitcnt lgkmcnt(0)
	v_add_f32_e32 v74, v74, v75
	v_cndmask_b32_e32 v1, v220, v76, vcc
	v_lshlrev_b32_e32 v1, 2, v1
	ds_bpermute_b32 v75, v1, v74
	s_waitcnt lgkmcnt(0)
	v_add_f32_e32 v70, v74, v75
	v_fmamk_f32 v70, v70, 0x3a000000, v221
	v_mul_f32_e32 v71, 0x4f800000, v70
	v_cmp_gt_f32_e32 vcc, s56, v70
	s_nop 1
	v_cndmask_b32_e32 v124, v70, v71, vcc
	v_sqrt_f32_e32 v216, v124
	global_load_dwordx4 v[94:97], v[126:127], off offset:512
	global_load_dwordx4 v[70:73], v[126:127], off offset:3072
	global_load_dwordx4 v[74:77], v[126:127], off offset:3328
	global_load_dwordx4 v[78:81], v[126:127], off offset:3584
	v_add_u32_e32 v217, -1, v216
	v_fma_f32 v226, -v217, v216, v124
	v_cmp_ge_f32_e64 s[6:7], 0, v226
	v_add_u32_e32 v226, 1, v216
	s_nop 0
	v_cndmask_b32_e64 v217, v216, v217, s[6:7]
	v_fma_f32 v216, -v226, v216, v124
	v_cmp_lt_f32_e64 s[6:7], 0, v216
	s_nop 1
	v_cndmask_b32_e64 v216, v217, v226, s[6:7]
	v_mul_f32_e32 v217, 0x37800000, v216
	v_cndmask_b32_e32 v216, v216, v217, vcc
	v_cmp_class_f32_e32 vcc, v124, v222
	s_nop 1
	v_cndmask_b32_e32 v124, v216, v124, vcc
	v_div_scale_f32 v216, s[6:7], v124, v124, 1.0
	v_rcp_f32_e32 v217, v216
	s_lshl_b64 s[6:7], s[54:55], 12
	v_fma_f32 v226, -v216, v217, 1.0
	v_fmac_f32_e32 v217, v226, v217
	v_div_scale_f32 v226, vcc, 1.0, v124, 1.0
	v_mul_f32_e32 v227, v226, v217
	v_fma_f32 v228, -v216, v227, v226
	v_fmac_f32_e32 v227, v228, v217
	v_fma_f32 v216, -v216, v227, v226
	v_div_fmas_f32 v216, v216, v217, v227
	v_div_fixup_f32 v124, v216, v124, 1.0
	v_pk_mul_f32 v[118:119], v[118:119], v[124:125] op_sel_hi:[1,0]
	v_pk_mul_f32 v[120:121], v[120:121], v[124:125] op_sel_hi:[1,0]
	v_pk_mul_f32 v[114:115], v[114:115], v[124:125] op_sel_hi:[1,0]
	v_pk_mul_f32 v[116:117], v[116:117], v[124:125] op_sel_hi:[1,0]
	v_pk_mul_f32 v[120:121], v[8:9], v[120:121]
	v_pk_mul_f32 v[118:119], v[6:7], v[118:119]
	v_pk_mul_f32 v[116:117], v[4:5], v[116:117]
	v_pk_mul_f32 v[114:115], v[2:3], v[114:115]
	v_lshl_add_u64 v[216:217], v[130:131], 0, s[6:7]
	v_cvt_pk_bf16_f32 v226, v118, v119
	v_cvt_pk_bf16_f32 v227, v120, v121
	v_cvt_pk_bf16_f32 v228, v114, v115
	v_cvt_pk_bf16_f32 v229, v116, v117
	v_pk_mul_f32 v[110:111], v[110:111], v[124:125] op_sel_hi:[1,0]
	v_pk_mul_f32 v[112:113], v[112:113], v[124:125] op_sel_hi:[1,0]
	v_pk_mul_f32 v[106:107], v[106:107], v[124:125] op_sel_hi:[1,0]
	v_pk_mul_f32 v[108:109], v[108:109], v[124:125] op_sel_hi:[1,0]
	global_store_dwordx4 v[216:217], v[226:229], off
	v_pk_mul_f32 v[112:113], v[16:17], v[112:113]
	v_pk_mul_f32 v[110:111], v[14:15], v[110:111]
	v_add_u32_e32 v226, s26, v122
	v_pk_mul_f32 v[108:109], v[12:13], v[108:109]
	v_pk_mul_f32 v[106:107], v[10:11], v[106:107]
	ds_write_b128 v226, v[118:121]
	ds_write_b128 v226, v[114:117] offset:16
	v_cvt_pk_bf16_f32 v114, v110, v111
	v_cvt_pk_bf16_f32 v115, v112, v113
	v_cvt_pk_bf16_f32 v116, v106, v107
	v_cvt_pk_bf16_f32 v117, v108, v109
	global_store_dwordx4 v[216:217], v[114:117], off offset:1024
	ds_write_b128 v226, v[110:113] offset:2048
	ds_write_b128 v226, v[106:109] offset:2064
	s_waitcnt vmcnt(15)
	v_mov_b32_e32 v108, v55
	s_waitcnt vmcnt(14)
	v_mov_b32_e32 v109, v51
	v_mov_b32_e32 v106, v54
	v_mov_b32_e32 v107, v50
	v_pk_mul_f32 v[108:109], v[108:109], v[108:109]
	v_mov_b32_e32 v110, v57
	v_mov_b32_e32 v111, v53
	v_pk_fma_f32 v[106:107], v[106:107], v[106:107], v[108:109]
	v_mov_b32_e32 v108, v56
	v_mov_b32_e32 v109, v52
	v_pk_mul_f32 v[110:111], v[110:111], v[110:111]
	v_pk_mul_f32 v[90:91], v[90:91], v[124:125] op_sel_hi:[1,0]
	v_pk_fma_f32 v[108:109], v[108:109], v[108:109], v[110:111]
	s_waitcnt vmcnt(12)
	v_pk_mul_f32 v[110:111], v[46:47], v[46:47]
	v_pk_add_f32 v[106:107], v[106:107], v[108:109]
	v_pk_mul_f32 v[108:109], v[48:49], v[48:49]
	v_pk_add_f32 v[106:107], v[106:107], v[106:107] op_sel:[0,1] op_sel_hi:[1,0]
	v_pk_mov_b32 v[112:113], v[110:111], v[108:109] op_sel:[1,0]
	v_mov_b32_e32 v111, v109
	v_pk_add_f32 v[108:109], v[112:113], v[110:111]
	s_waitcnt vmcnt(11)
	v_mul_f32_e32 v110, v38, v38
	v_mul_f32_e32 v111, v39, v39
	v_pk_add_f32 v[108:109], v[108:109], v[108:109] op_sel:[0,1] op_sel_hi:[1,0]
	v_mov_b32_e32 v107, v110
	v_mov_b32_e32 v109, v111
	v_pk_add_f32 v[106:107], v[106:107], v[108:109]
	v_mul_f32_e32 v108, v43, v43
	v_mul_f32_e32 v110, v45, v45
	v_mul_f32_e32 v112, v40, v40
	v_mul_f32_e32 v113, v41, v41
	v_pk_fma_f32 v[108:109], v[42:43], v[42:43], v[108:109] op_sel_hi:[1,1,0]
	v_pk_fma_f32 v[110:111], v[44:45], v[44:45], v[110:111] op_sel_hi:[1,1,0]
	v_mov_b32_e32 v109, v112
	v_mov_b32_e32 v111, v113
	v_pk_add_f32 v[108:109], v[108:109], v[110:111]
	s_waitcnt vmcnt(10)
	v_pk_mul_f32 v[110:111], v[34:35], v[34:35]
	v_pk_add_f32 v[106:107], v[106:107], v[108:109]
	v_pk_mul_f32 v[108:109], v[36:37], v[36:37]
	v_pk_add_f32 v[106:107], v[106:107], v[106:107] op_sel:[0,1] op_sel_hi:[1,0]
	v_pk_mov_b32 v[112:113], v[110:111], v[108:109] op_sel:[1,0]
	v_mov_b32_e32 v111, v109
	v_pk_add_f32 v[108:109], v[112:113], v[110:111]
	s_waitcnt vmcnt(8)
	v_mul_f32_e32 v110, v98, v98
	v_mul_f32_e32 v111, v99, v99
	v_pk_add_f32 v[108:109], v[108:109], v[108:109] op_sel:[0,1] op_sel_hi:[1,0]
	v_mov_b32_e32 v107, v110
	v_mov_b32_e32 v109, v111
	v_pk_add_f32 v[106:107], v[106:107], v[108:109]
	v_mul_f32_e32 v108, v103, v103
	v_mul_f32_e32 v110, v105, v105
	v_mul_f32_e32 v112, v100, v100
	v_mul_f32_e32 v113, v101, v101
	v_pk_fma_f32 v[108:109], v[102:103], v[102:103], v[108:109] op_sel_hi:[1,1,0]
	v_pk_fma_f32 v[110:111], v[104:105], v[104:105], v[110:111] op_sel_hi:[1,1,0]
	v_mov_b32_e32 v109, v112
	v_mov_b32_e32 v111, v113
	v_pk_add_f32 v[108:109], v[108:109], v[110:111]
	v_pk_mul_f32 v[92:93], v[92:93], v[124:125] op_sel_hi:[1,0]
	v_pk_add_f32 v[106:107], v[106:107], v[108:109]
	v_pk_mul_f32 v[66:67], v[66:67], v[124:125] op_sel_hi:[1,0]
	v_add_f32_e32 v106, v106, v107
	ds_bpermute_b32 v107, v218, v106
	v_pk_mul_f32 v[68:69], v[68:69], v[124:125] op_sel_hi:[1,0]
	v_pk_mul_f32 v[92:93], v[20:21], v[92:93]
	v_pk_mul_f32 v[90:91], v[18:19], v[90:91]
	v_pk_mul_f32 v[68:69], v[28:29], v[68:69]
	s_waitcnt lgkmcnt(0)
	v_add_f32_e32 v107, v106, v107
	ds_bpermute_b32 v108, v225, v107
	v_pk_mul_f32 v[66:67], v[26:27], v[66:67]
	v_cvt_pk_bf16_f32 v106, v90, v91
	v_cvt_pk_bf16_f32 v109, v68, v69
	v_pk_mul_f32 v[62:63], v[62:63], v[124:125] op_sel_hi:[1,0]
	s_waitcnt lgkmcnt(0)
	v_add_f32_e32 v110, v107, v108
	ds_bpermute_b32 v111, v230, v110
	v_cvt_pk_bf16_f32 v107, v92, v93
	v_cvt_pk_bf16_f32 v108, v66, v67
	global_store_dwordx4 v[216:217], v[106:109], off offset:2048
	ds_write_b128 v226, v[90:93] offset:4096
	ds_write_b128 v226, v[66:69] offset:4112
	s_waitcnt lgkmcnt(2)
	v_add_f32_e32 v106, v110, v111
	ds_bpermute_b32 v107, v231, v106
	v_pk_mul_f32 v[64:65], v[64:65], v[124:125] op_sel_hi:[1,0]
	v_pk_mul_f32 v[58:59], v[58:59], v[124:125] op_sel_hi:[1,0]
	v_pk_mul_f32 v[60:61], v[60:61], v[124:125] op_sel_hi:[1,0]
	v_pk_mul_f32 v[64:65], v[24:25], v[64:65]
	s_waitcnt lgkmcnt(0)
	v_add_f32_e32 v66, v106, v107
	ds_bpermute_b32 v67, v232, v66
	v_pk_mul_f32 v[62:63], v[22:23], v[62:63]
	v_pk_mul_f32 v[60:61], v[32:33], v[60:61]
	v_pk_mul_f32 v[58:59], v[30:31], v[58:59]
	v_cvt_pk_bf16_f32 v69, v60, v61
	s_waitcnt lgkmcnt(0)
	v_add_f32_e32 v68, v66, v67
	ds_bpermute_b32 v1, v1, v68
	v_cvt_pk_bf16_f32 v66, v62, v63
	v_cvt_pk_bf16_f32 v67, v64, v65
	s_waitcnt lgkmcnt(0)
	v_add_f32_e32 v1, v68, v1
	v_fmamk_f32 v1, v1, 0x3a000000, v221
	v_mul_f32_e32 v68, 0x4f800000, v1
	v_cmp_gt_f32_e32 vcc, s56, v1
	s_nop 1
	v_cndmask_b32_e32 v1, v1, v68, vcc
	v_sqrt_f32_e32 v90, v1
	v_cvt_pk_bf16_f32 v68, v58, v59
	global_store_dwordx4 v[216:217], v[66:69], off offset:3072
	ds_write_b128 v226, v[62:65] offset:6144
	ds_write_b128 v226, v[58:61] offset:6160
	v_add_u32_e32 v66, -1, v90
	v_fma_f32 v67, -v66, v90, v1
	v_cmp_ge_f32_e64 s[6:7], 0, v67
	v_add_u32_e32 v67, 1, v90
	v_fma_f32 v68, -v67, v90, v1
	v_cndmask_b32_e64 v66, v90, v66, s[6:7]
	v_cmp_lt_f32_e64 s[6:7], 0, v68
	s_nop 1
	v_cndmask_b32_e64 v66, v66, v67, s[6:7]
	v_mul_f32_e32 v67, 0x37800000, v66
	v_cndmask_b32_e32 v66, v66, v67, vcc
	v_cmp_class_f32_e32 vcc, v1, v222
	s_nop 1
	v_cndmask_b32_e32 v1, v66, v1, vcc
	v_div_scale_f32 v66, s[6:7], v1, v1, 1.0
	v_rcp_f32_e32 v67, v66
	s_lshl_b64 s[6:7], s[58:59], 12
	v_lshl_add_u64 v[64:65], v[130:131], 0, s[6:7]
	v_fma_f32 v58, -v66, v67, 1.0
	v_fmac_f32_e32 v67, v58, v67
	v_div_scale_f32 v58, vcc, 1.0, v1, 1.0
	v_mul_f32_e32 v59, v58, v67
	v_fma_f32 v60, -v66, v59, v58
	v_fmac_f32_e32 v59, v60, v67
	v_fma_f32 v58, -v66, v59, v58
	v_div_fmas_f32 v58, v58, v67, v59
	v_div_fixup_f32 v62, v58, v1, 1.0
	v_pk_mul_f32 v[54:55], v[54:55], v[62:63] op_sel_hi:[1,0]
	v_pk_mul_f32 v[56:57], v[56:57], v[62:63] op_sel_hi:[1,0]
	v_pk_mul_f32 v[50:51], v[50:51], v[62:63] op_sel_hi:[1,0]
	v_pk_mul_f32 v[52:53], v[52:53], v[62:63] op_sel_hi:[1,0]
	v_pk_mul_f32 v[56:57], v[8:9], v[56:57]
	v_pk_mul_f32 v[54:55], v[6:7], v[54:55]
	v_pk_mul_f32 v[52:53], v[4:5], v[52:53]
	v_pk_mul_f32 v[50:51], v[2:3], v[50:51]
	v_pk_mul_f32 v[46:47], v[46:47], v[62:63] op_sel_hi:[1,0]
	v_pk_mul_f32 v[48:49], v[48:49], v[62:63] op_sel_hi:[1,0]
	v_pk_mul_f32 v[42:43], v[42:43], v[62:63] op_sel_hi:[1,0]
	v_pk_mul_f32 v[44:45], v[44:45], v[62:63] op_sel_hi:[1,0]
	v_cvt_pk_bf16_f32 v58, v54, v55
	v_cvt_pk_bf16_f32 v59, v56, v57
	v_cvt_pk_bf16_f32 v60, v50, v51
	v_cvt_pk_bf16_f32 v61, v52, v53
	v_add_u32_e32 v1, s33, v122
	v_pk_mul_f32 v[48:49], v[16:17], v[48:49]
	v_pk_mul_f32 v[46:47], v[14:15], v[46:47]
	v_pk_mul_f32 v[44:45], v[12:13], v[44:45]
	v_pk_mul_f32 v[42:43], v[10:11], v[42:43]
	v_pk_mul_f32 v[38:39], v[38:39], v[62:63] op_sel_hi:[1,0]
	v_pk_mul_f32 v[40:41], v[40:41], v[62:63] op_sel_hi:[1,0]
	v_pk_mul_f32 v[34:35], v[34:35], v[62:63] op_sel_hi:[1,0]
	v_pk_mul_f32 v[36:37], v[36:37], v[62:63] op_sel_hi:[1,0]
	global_store_dwordx4 v[64:65], v[58:61], off
	ds_write_b128 v1, v[54:57]
	ds_write_b128 v1, v[50:53] offset:16
	v_cvt_pk_bf16_f32 v50, v46, v47
	v_cvt_pk_bf16_f32 v51, v48, v49
	v_cvt_pk_bf16_f32 v52, v42, v43
	v_cvt_pk_bf16_f32 v53, v44, v45
	v_pk_mul_f32 v[40:41], v[20:21], v[40:41]
	v_pk_mul_f32 v[38:39], v[18:19], v[38:39]
	v_pk_mul_f32 v[36:37], v[28:29], v[36:37]
	v_pk_mul_f32 v[34:35], v[26:27], v[34:35]
	global_store_dwordx4 v[64:65], v[50:53], off offset:1024
	ds_write_b128 v1, v[46:49] offset:2048
	ds_write_b128 v1, v[42:45] offset:2064
	v_cvt_pk_bf16_f32 v42, v38, v39
	v_cvt_pk_bf16_f32 v43, v40, v41
	v_cvt_pk_bf16_f32 v44, v34, v35
	v_cvt_pk_bf16_f32 v45, v36, v37
	global_store_dwordx4 v[64:65], v[42:45], off offset:2048
	ds_write_b128 v1, v[38:41] offset:4096
	ds_write_b128 v1, v[34:37] offset:4112
	v_pk_mul_f32 v[34:35], v[102:103], v[62:63] op_sel_hi:[1,0]
	v_pk_mul_f32 v[36:37], v[104:105], v[62:63] op_sel_hi:[1,0]
	v_pk_mul_f32 v[38:39], v[98:99], v[62:63] op_sel_hi:[1,0]
	v_pk_mul_f32 v[40:41], v[100:101], v[62:63] op_sel_hi:[1,0]
	v_pk_mul_f32 v[36:37], v[24:25], v[36:37]
	v_pk_mul_f32 v[34:35], v[22:23], v[34:35]
	v_pk_mul_f32 v[40:41], v[32:33], v[40:41]
	v_pk_mul_f32 v[38:39], v[30:31], v[38:39]
	v_cvt_pk_bf16_f32 v42, v34, v35
	v_cvt_pk_bf16_f32 v43, v36, v37
	v_cvt_pk_bf16_f32 v44, v38, v39
	v_cvt_pk_bf16_f32 v45, v40, v41
	global_store_dwordx4 v[64:65], v[42:45], off offset:3072
	ds_write_b128 v1, v[34:37] offset:6144
	ds_write_b128 v1, v[38:41] offset:6160
	s_waitcnt lgkmcnt(0)
	s_barrier
	global_load_dwordx4 v[34:37], v[132:133], off
	global_load_dwordx4 v[38:41], v[134:135], off
	global_load_dwordx4 v[42:45], v[136:137], off
	global_load_dwordx4 v[46:49], v[138:139], off
	global_load_dwordx4 v[50:53], v[140:141], off
	global_load_dwordx4 v[54:57], v[142:143], off
	global_load_dwordx4 v[58:61], v[144:145], off
	global_load_dwordx4 v[62:65], v[146:147], off
	global_load_dwordx4 v[66:69], v[148:149], off
	global_load_dwordx4 v[90:93], v[150:151], off
	global_load_dwordx4 v[98:101], v[152:153], off
	global_load_dwordx4 v[102:105], v[154:155], off
	global_load_dwordx4 v[106:109], v[156:157], off
	global_load_dwordx4 v[110:113], v[158:159], off
	global_load_dwordx4 v[114:117], v[160:161], off
	global_load_dwordx4 v[118:121], v[162:163], off
	global_load_dwordx4 v[226:229], v[164:165], off
	global_load_dwordx4 v[230:233], v[166:167], off
	ds_read_b128 v[234:237], v123
	ds_read_b128 v[238:241], v123 offset:64
	s_waitcnt vmcnt(31) lgkmcnt(1)
	v_mfma_f32_16x16x4_f32 v[242:245], v234, v82, 0
	s_waitcnt vmcnt(30)
	v_mfma_f32_16x16x4_f32 v[246:249], v234, v86, 0
	s_waitcnt vmcnt(29)
	v_mfma_f32_16x16x4_f32 v[250:253], v234, v94, 0
	v_mfma_f32_16x16x4_f32 v[242:245], v235, v83, v[242:245]
	v_mfma_f32_16x16x4_f32 v[246:249], v235, v87, v[246:249]
	v_mfma_f32_16x16x4_f32 v[250:253], v235, v95, v[250:253]
	v_mfma_f32_16x16x4_f32 v[242:245], v236, v84, v[242:245]
	v_mfma_f32_16x16x4_f32 v[246:249], v236, v88, v[246:249]
	v_mfma_f32_16x16x4_f32 v[250:253], v236, v96, v[250:253]
	v_mfma_f32_16x16x4_f32 v[82:85], v237, v85, v[242:245]
	v_mfma_f32_16x16x4_f32 v[86:89], v237, v89, v[246:249]
	v_mfma_f32_16x16x4_f32 v[94:97], v237, v97, v[250:253]
	s_waitcnt vmcnt(28) lgkmcnt(0)
	v_mfma_f32_16x16x4_f32 v[82:85], v238, v70, v[82:85]
	s_waitcnt vmcnt(27)
	v_mfma_f32_16x16x4_f32 v[86:89], v238, v74, v[86:89]
	s_waitcnt vmcnt(26)
	v_mfma_f32_16x16x4_f32 v[94:97], v238, v78, v[94:97]
	v_mfma_f32_16x16x4_f32 v[82:85], v239, v71, v[82:85]
	v_mfma_f32_16x16x4_f32 v[86:89], v239, v75, v[86:89]
	v_mfma_f32_16x16x4_f32 v[94:97], v239, v79, v[94:97]
	v_mfma_f32_16x16x4_f32 v[82:85], v240, v72, v[82:85]
	v_mfma_f32_16x16x4_f32 v[86:89], v240, v76, v[86:89]
	v_mfma_f32_16x16x4_f32 v[94:97], v240, v80, v[94:97]
	v_mfma_f32_16x16x4_f32 v[70:73], v241, v73, v[82:85]
	v_mfma_f32_16x16x4_f32 v[74:77], v241, v77, v[86:89]
	s_nop 5
	ds_read_b128 v[82:85], v123 offset:128
	ds_read_b128 v[86:89], v123 offset:192
	v_mfma_f32_16x16x4_f32 v[78:81], v241, v81, v[94:97]
	s_waitcnt vmcnt(17) lgkmcnt(1)
	v_mfma_f32_16x16x4_f32 v[70:73], v82, v34, v[70:73]
	s_waitcnt vmcnt(16)
	v_mfma_f32_16x16x4_f32 v[74:77], v82, v38, v[74:77]
	s_waitcnt vmcnt(15)
	v_mfma_f32_16x16x4_f32 v[78:81], v82, v42, v[78:81]
	v_mfma_f32_16x16x4_f32 v[70:73], v83, v35, v[70:73]
	v_mfma_f32_16x16x4_f32 v[74:77], v83, v39, v[74:77]
	v_mfma_f32_16x16x4_f32 v[78:81], v83, v43, v[78:81]
	v_mfma_f32_16x16x4_f32 v[70:73], v84, v36, v[70:73]
	v_mfma_f32_16x16x4_f32 v[74:77], v84, v40, v[74:77]
	v_mfma_f32_16x16x4_f32 v[78:81], v84, v44, v[78:81]
	v_mfma_f32_16x16x4_f32 v[34:37], v85, v37, v[70:73]
	v_mfma_f32_16x16x4_f32 v[38:41], v85, v41, v[74:77]
	v_mfma_f32_16x16x4_f32 v[42:45], v85, v45, v[78:81]
	s_waitcnt vmcnt(12) lgkmcnt(0)
	v_mfma_f32_16x16x4_f32 v[42:45], v86, v54, v[42:45]
	v_mfma_f32_16x16x4_f32 v[34:37], v86, v46, v[34:37]
	v_mfma_f32_16x16x4_f32 v[38:41], v86, v50, v[38:41]
	v_mfma_f32_16x16x4_f32 v[42:45], v87, v55, v[42:45]
	v_mfma_f32_16x16x4_f32 v[34:37], v87, v47, v[34:37]
	v_mfma_f32_16x16x4_f32 v[38:41], v87, v51, v[38:41]
	v_mfma_f32_16x16x4_f32 v[42:45], v88, v56, v[42:45]
	v_mfma_f32_16x16x4_f32 v[34:37], v88, v48, v[34:37]
	v_mfma_f32_16x16x4_f32 v[38:41], v88, v52, v[38:41]
	v_mfma_f32_16x16x4_f32 v[34:37], v89, v49, v[34:37]
	global_load_dwordx4 v[46:49], v[168:169], off
	global_load_dwordx4 v[70:73], v[170:171], off
	global_load_dwordx4 v[74:77], v[172:173], off
	global_load_dwordx4 v[78:81], v[174:175], off
	v_mfma_f32_16x16x4_f32 v[38:41], v89, v53, v[38:41]
	global_load_dwordx4 v[50:53], v[176:177], off
	global_load_dwordx4 v[82:85], v[178:179], off
	global_load_dwordx4 v[94:97], v[180:181], off
	global_load_dwordx4 v[234:237], v[182:183], off
	global_load_dwordx4 v[238:241], v[184:185], off
	global_load_dwordx4 v[242:245], v[186:187], off
	global_load_dwordx4 v[246:249], v[188:189], off
	global_load_dwordx4 v[250:253], v[190:191], off
	v_mfma_f32_16x16x4_f32 v[42:45], v89, v57, v[42:45]
	ds_read_b128 v[54:57], v123 offset:256
	ds_read_b128 v[86:89], v123 offset:320
	s_waitcnt vmcnt(23) lgkmcnt(1)
	v_mfma_f32_16x16x4_f32 v[34:37], v54, v58, v[34:37]
	s_waitcnt vmcnt(22)
	v_mfma_f32_16x16x4_f32 v[38:41], v54, v62, v[38:41]
	s_waitcnt vmcnt(21)
	v_mfma_f32_16x16x4_f32 v[42:45], v54, v66, v[42:45]
	v_mfma_f32_16x16x4_f32 v[34:37], v55, v59, v[34:37]
	v_mfma_f32_16x16x4_f32 v[38:41], v55, v63, v[38:41]
	v_mfma_f32_16x16x4_f32 v[42:45], v55, v67, v[42:45]
	v_mfma_f32_16x16x4_f32 v[34:37], v56, v60, v[34:37]
	v_mfma_f32_16x16x4_f32 v[38:41], v56, v64, v[38:41]
	v_mfma_f32_16x16x4_f32 v[42:45], v56, v68, v[42:45]
	v_mfma_f32_16x16x4_f32 v[34:37], v57, v61, v[34:37]
	v_mfma_f32_16x16x4_f32 v[38:41], v57, v65, v[38:41]
	v_mfma_f32_16x16x4_f32 v[42:45], v57, v69, v[42:45]
	ds_read_b128 v[54:57], v123 offset:384
	ds_read_b128 v[58:61], v123 offset:448
	s_waitcnt vmcnt(20) lgkmcnt(2)
	v_mfma_f32_16x16x4_f32 v[34:37], v86, v90, v[34:37]
	s_waitcnt vmcnt(19)
	v_mfma_f32_16x16x4_f32 v[38:41], v86, v98, v[38:41]
	s_waitcnt vmcnt(18)
	v_mfma_f32_16x16x4_f32 v[42:45], v86, v102, v[42:45]
	v_mfma_f32_16x16x4_f32 v[34:37], v87, v91, v[34:37]
	v_mfma_f32_16x16x4_f32 v[38:41], v87, v99, v[38:41]
	v_mfma_f32_16x16x4_f32 v[42:45], v87, v103, v[42:45]
	v_mfma_f32_16x16x4_f32 v[34:37], v88, v92, v[34:37]
	v_mfma_f32_16x16x4_f32 v[38:41], v88, v100, v[38:41]
	v_mfma_f32_16x16x4_f32 v[42:45], v88, v104, v[42:45]
	v_mfma_f32_16x16x4_f32 v[34:37], v89, v93, v[34:37]
	v_mfma_f32_16x16x4_f32 v[38:41], v89, v101, v[38:41]
	v_mfma_f32_16x16x4_f32 v[42:45], v89, v105, v[42:45]
	s_waitcnt vmcnt(17) lgkmcnt(1)
	v_mfma_f32_16x16x4_f32 v[34:37], v54, v106, v[34:37]
	s_waitcnt vmcnt(16)
	v_mfma_f32_16x16x4_f32 v[38:41], v54, v110, v[38:41]
	s_waitcnt vmcnt(15)
	v_mfma_f32_16x16x4_f32 v[42:45], v54, v114, v[42:45]
	v_mfma_f32_16x16x4_f32 v[34:37], v55, v107, v[34:37]
	v_mfma_f32_16x16x4_f32 v[38:41], v55, v111, v[38:41]
	v_mfma_f32_16x16x4_f32 v[42:45], v55, v115, v[42:45]
	v_mfma_f32_16x16x4_f32 v[34:37], v56, v108, v[34:37]
	v_mfma_f32_16x16x4_f32 v[38:41], v56, v112, v[38:41]
	v_mfma_f32_16x16x4_f32 v[42:45], v56, v116, v[42:45]
	v_mfma_f32_16x16x4_f32 v[34:37], v57, v109, v[34:37]
	v_mfma_f32_16x16x4_f32 v[38:41], v57, v113, v[38:41]
	v_mfma_f32_16x16x4_f32 v[42:45], v57, v117, v[42:45]
	global_load_dwordx4 v[54:57], v[192:193], off
	global_load_dwordx4 v[62:65], v[194:195], off
	global_load_dwordx4 v[66:69], v[196:197], off
	global_load_dwordx4 v[86:89], v[198:199], off
	s_waitcnt vmcnt(16) lgkmcnt(0)
	v_mfma_f32_16x16x4_f32 v[42:45], v58, v230, v[42:45]
	v_mfma_f32_16x16x4_f32 v[34:37], v58, v118, v[34:37]
	v_mfma_f32_16x16x4_f32 v[38:41], v58, v226, v[38:41]
	v_mfma_f32_16x16x4_f32 v[42:45], v59, v231, v[42:45]
	v_mfma_f32_16x16x4_f32 v[34:37], v59, v119, v[34:37]
	v_mfma_f32_16x16x4_f32 v[38:41], v59, v227, v[38:41]
	v_mfma_f32_16x16x4_f32 v[42:45], v60, v232, v[42:45]
	v_mfma_f32_16x16x4_f32 v[34:37], v60, v120, v[34:37]
	v_mfma_f32_16x16x4_f32 v[38:41], v60, v228, v[38:41]
	v_mfma_f32_16x16x4_f32 v[34:37], v61, v121, v[34:37]
	v_mfma_f32_16x16x4_f32 v[38:41], v61, v229, v[38:41]
	global_load_dwordx4 v[90:93], v[200:201], off
	global_load_dwordx4 v[98:101], v[202:203], off
	global_load_dwordx4 v[102:105], v[204:205], off
	global_load_dwordx4 v[106:109], v[206:207], off
	global_load_dwordx4 v[110:113], v[208:209], off
	global_load_dwordx4 v[114:117], v[210:211], off
	global_load_dwordx4 v[118:121], v[212:213], off
	global_load_dwordx4 v[226:229], v[214:215], off
	v_mfma_f32_16x16x4_f32 v[42:45], v61, v233, v[42:45]
	ds_read_b128 v[58:61], v123 offset:512
	ds_read_b128 v[230:233], v123 offset:576
	s_waitcnt vmcnt(23) lgkmcnt(1)
	v_mfma_f32_16x16x4_f32 v[34:37], v58, v46, v[34:37]
	s_waitcnt vmcnt(22)
	v_mfma_f32_16x16x4_f32 v[38:41], v58, v70, v[38:41]
	s_waitcnt vmcnt(21)
	v_mfma_f32_16x16x4_f32 v[42:45], v58, v74, v[42:45]
	v_mfma_f32_16x16x4_f32 v[34:37], v59, v47, v[34:37]
	v_mfma_f32_16x16x4_f32 v[38:41], v59, v71, v[38:41]
	v_mfma_f32_16x16x4_f32 v[42:45], v59, v75, v[42:45]
	v_mfma_f32_16x16x4_f32 v[34:37], v60, v48, v[34:37]
	v_mfma_f32_16x16x4_f32 v[38:41], v60, v72, v[38:41]
	v_mfma_f32_16x16x4_f32 v[42:45], v60, v76, v[42:45]
	v_mfma_f32_16x16x4_f32 v[34:37], v61, v49, v[34:37]
	v_mfma_f32_16x16x4_f32 v[38:41], v61, v73, v[38:41]
	v_mfma_f32_16x16x4_f32 v[42:45], v61, v77, v[42:45]
	s_waitcnt vmcnt(20) lgkmcnt(0)
	v_mfma_f32_16x16x4_f32 v[34:37], v230, v78, v[34:37]
	s_waitcnt vmcnt(19)
	v_mfma_f32_16x16x4_f32 v[38:41], v230, v50, v[38:41]
	s_waitcnt vmcnt(18)
	v_mfma_f32_16x16x4_f32 v[42:45], v230, v82, v[42:45]
	v_mfma_f32_16x16x4_f32 v[34:37], v231, v79, v[34:37]
	v_mfma_f32_16x16x4_f32 v[38:41], v231, v51, v[38:41]
	v_mfma_f32_16x16x4_f32 v[42:45], v231, v83, v[42:45]
	v_mfma_f32_16x16x4_f32 v[34:37], v232, v80, v[34:37]
	v_mfma_f32_16x16x4_f32 v[38:41], v232, v52, v[38:41]
	v_mfma_f32_16x16x4_f32 v[42:45], v232, v84, v[42:45]
	v_mfma_f32_16x16x4_f32 v[34:37], v233, v81, v[34:37]
	v_mfma_f32_16x16x4_f32 v[38:41], v233, v53, v[38:41]
	ds_read_b128 v[46:49], v123 offset:640
	ds_read_b128 v[50:53], v123 offset:704
	v_mfma_f32_16x16x4_f32 v[42:45], v233, v85, v[42:45]
	s_waitcnt vmcnt(17) lgkmcnt(1)
	v_mfma_f32_16x16x4_f32 v[34:37], v46, v94, v[34:37]
	s_waitcnt vmcnt(16)
	v_mfma_f32_16x16x4_f32 v[38:41], v46, v234, v[38:41]
	s_waitcnt vmcnt(15)
	v_mfma_f32_16x16x4_f32 v[42:45], v46, v238, v[42:45]
	v_mfma_f32_16x16x4_f32 v[34:37], v47, v95, v[34:37]
	v_mfma_f32_16x16x4_f32 v[38:41], v47, v235, v[38:41]
	v_mfma_f32_16x16x4_f32 v[42:45], v47, v239, v[42:45]
	v_mfma_f32_16x16x4_f32 v[34:37], v48, v96, v[34:37]
	v_mfma_f32_16x16x4_f32 v[38:41], v48, v236, v[38:41]
	v_mfma_f32_16x16x4_f32 v[42:45], v48, v240, v[42:45]
	v_mfma_f32_16x16x4_f32 v[34:37], v49, v97, v[34:37]
	v_mfma_f32_16x16x4_f32 v[38:41], v49, v237, v[38:41]
	v_mfma_f32_16x16x4_f32 v[42:45], v49, v241, v[42:45]
	s_waitcnt vmcnt(14) lgkmcnt(0)
	v_mfma_f32_16x16x4_f32 v[34:37], v50, v242, v[34:37]
	s_waitcnt vmcnt(13)
	v_mfma_f32_16x16x4_f32 v[38:41], v50, v246, v[38:41]
	s_waitcnt vmcnt(12)
	v_mfma_f32_16x16x4_f32 v[42:45], v50, v250, v[42:45]
	v_mfma_f32_16x16x4_f32 v[34:37], v51, v243, v[34:37]
	v_mfma_f32_16x16x4_f32 v[38:41], v51, v247, v[38:41]
	v_mfma_f32_16x16x4_f32 v[42:45], v51, v251, v[42:45]
	v_mfma_f32_16x16x4_f32 v[34:37], v52, v244, v[34:37]
	v_mfma_f32_16x16x4_f32 v[38:41], v52, v248, v[38:41]
	v_mfma_f32_16x16x4_f32 v[42:45], v52, v252, v[42:45]
	v_mfma_f32_16x16x4_f32 v[34:37], v53, v245, v[34:37]
	v_mfma_f32_16x16x4_f32 v[38:41], v53, v249, v[38:41]
	v_mfma_f32_16x16x4_f32 v[42:45], v53, v253, v[42:45]
	ds_read_b128 v[46:49], v123 offset:768
	ds_read_b128 v[50:53], v123 offset:832
	s_waitcnt vmcnt(11) lgkmcnt(1)
	v_mfma_f32_16x16x4_f32 v[34:37], v46, v54, v[34:37]
	s_waitcnt vmcnt(10)
	v_mfma_f32_16x16x4_f32 v[38:41], v46, v62, v[38:41]
	s_waitcnt vmcnt(9)
	v_mfma_f32_16x16x4_f32 v[42:45], v46, v66, v[42:45]
	v_mfma_f32_16x16x4_f32 v[34:37], v47, v55, v[34:37]
	v_mfma_f32_16x16x4_f32 v[38:41], v47, v63, v[38:41]
	v_mfma_f32_16x16x4_f32 v[42:45], v47, v67, v[42:45]
	v_mfma_f32_16x16x4_f32 v[34:37], v48, v56, v[34:37]
	v_mfma_f32_16x16x4_f32 v[38:41], v48, v64, v[38:41]
	v_mfma_f32_16x16x4_f32 v[42:45], v48, v68, v[42:45]
	v_mfma_f32_16x16x4_f32 v[34:37], v49, v57, v[34:37]
	v_mfma_f32_16x16x4_f32 v[38:41], v49, v65, v[38:41]
	v_mfma_f32_16x16x4_f32 v[42:45], v49, v69, v[42:45]
	s_waitcnt vmcnt(8) lgkmcnt(0)
	v_mfma_f32_16x16x4_f32 v[34:37], v50, v86, v[34:37]
	s_waitcnt vmcnt(7)
	v_mfma_f32_16x16x4_f32 v[38:41], v50, v90, v[38:41]
	s_waitcnt vmcnt(6)
	v_mfma_f32_16x16x4_f32 v[42:45], v50, v98, v[42:45]
	v_mfma_f32_16x16x4_f32 v[34:37], v51, v87, v[34:37]
	v_mfma_f32_16x16x4_f32 v[38:41], v51, v91, v[38:41]
	v_mfma_f32_16x16x4_f32 v[42:45], v51, v99, v[42:45]
	v_mfma_f32_16x16x4_f32 v[34:37], v52, v88, v[34:37]
	v_mfma_f32_16x16x4_f32 v[38:41], v52, v92, v[38:41]
	v_mfma_f32_16x16x4_f32 v[42:45], v52, v100, v[42:45]
	v_mfma_f32_16x16x4_f32 v[34:37], v53, v89, v[34:37]
	v_mfma_f32_16x16x4_f32 v[38:41], v53, v93, v[38:41]
	v_mfma_f32_16x16x4_f32 v[42:45], v53, v101, v[42:45]
	ds_read_b128 v[46:49], v123 offset:896
	ds_read_b128 v[50:53], v123 offset:960
	s_waitcnt vmcnt(5) lgkmcnt(1)
	v_mfma_f32_16x16x4_f32 v[34:37], v46, v102, v[34:37]
	s_waitcnt vmcnt(4)
	v_mfma_f32_16x16x4_f32 v[38:41], v46, v106, v[38:41]
	s_waitcnt vmcnt(3)
	v_mfma_f32_16x16x4_f32 v[42:45], v46, v110, v[42:45]
	v_mfma_f32_16x16x4_f32 v[34:37], v47, v103, v[34:37]
	v_mfma_f32_16x16x4_f32 v[38:41], v47, v107, v[38:41]
	v_mfma_f32_16x16x4_f32 v[42:45], v47, v111, v[42:45]
	v_mfma_f32_16x16x4_f32 v[34:37], v48, v104, v[34:37]
	v_mfma_f32_16x16x4_f32 v[38:41], v48, v108, v[38:41]
	v_mfma_f32_16x16x4_f32 v[42:45], v48, v112, v[42:45]
	v_mfma_f32_16x16x4_f32 v[34:37], v49, v105, v[34:37]
	v_mfma_f32_16x16x4_f32 v[38:41], v49, v109, v[38:41]
	v_mfma_f32_16x16x4_f32 v[42:45], v49, v113, v[42:45]
	s_waitcnt vmcnt(2) lgkmcnt(0)
	v_mfma_f32_16x16x4_f32 v[34:37], v50, v114, v[34:37]
	s_waitcnt vmcnt(1)
	v_mfma_f32_16x16x4_f32 v[38:41], v50, v118, v[38:41]
	s_waitcnt vmcnt(0)
	v_mfma_f32_16x16x4_f32 v[42:45], v50, v226, v[42:45]
	v_mfma_f32_16x16x4_f32 v[34:37], v51, v115, v[34:37]
	v_mfma_f32_16x16x4_f32 v[38:41], v51, v119, v[38:41]
	v_mfma_f32_16x16x4_f32 v[42:45], v51, v227, v[42:45]
	v_mfma_f32_16x16x4_f32 v[34:37], v52, v116, v[34:37]
	v_mfma_f32_16x16x4_f32 v[38:41], v52, v120, v[38:41]
	v_mfma_f32_16x16x4_f32 v[42:45], v52, v228, v[42:45]
	v_mfma_f32_16x16x4_f32 v[34:37], v53, v117, v[34:37]
	v_mfma_f32_16x16x4_f32 v[38:41], v53, v121, v[38:41]
	v_mfma_f32_16x16x4_f32 v[42:45], v53, v229, v[42:45]
	s_cmp_gt_u32 s68, 2
	s_cbranch_scc1 .Lrpf_a_skip
	s_add_i32 s82, s68, 1
	s_lshl_b32 s82, s82, 4
	s_add_i32 s82, s67, s82
	s_ashr_i32 s83, s82, 31
	s_lshl_b64 s[82:83], s[82:83], 13
	v_lshl_add_u64 v[98:99], v[128:129], 0, s[82:83]
	s_add_u32 s82, s82, 0x1000
	s_addc_u32 s83, s83, 0
	global_load_dwordx4 v[118:121], v[98:99], off
	global_load_dwordx4 v[114:117], v[98:99], off offset:16
	global_load_dwordx4 v[110:113], v[98:99], off offset:2048
	global_load_dwordx4 v[106:109], v[98:99], off offset:2064
	v_lshl_add_u64 v[100:101], v[128:129], 0, s[82:83]
	s_add_u32 s82, s82, 0x1000
	s_addc_u32 s83, s83, 0
	global_load_dwordx4 v[58:61], v[100:101], off offset:2064
	global_load_dwordx4 v[90:93], v[100:101], off
	global_load_dwordx4 v[66:69], v[100:101], off offset:16
	global_load_dwordx4 v[62:65], v[100:101], off offset:2048
	v_lshl_add_u64 v[98:99], v[128:129], 0, s[82:83]
	s_nop 0
	global_load_dwordx4 v[54:57], v[98:99], off
	global_load_dwordx4 v[50:53], v[98:99], off offset:16
.Lrpf_a_skip:
	s_nop 8
	ds_write2_b32 v223, v34, v38 offset1:16
	ds_write2_b32 v223, v42, v35 offset0:32 offset1:48
	ds_write2_b32 v223, v39, v43 offset0:64 offset1:80
	ds_write2_b32 v223, v36, v40 offset0:96 offset1:112
	ds_write2_b32 v223, v44, v37 offset0:128 offset1:144
	ds_write2_b32 v223, v41, v45 offset0:160 offset1:176
	s_waitcnt lgkmcnt(0)
	s_barrier
	s_and_saveexec_b64 s[6:7], s[4:5]
	s_cbranch_execz .LBB0_595
	s_mov_b64 s[8:9], 0
	v_mov_b32_e32 v34, v0
.LBB0_594:
	v_mul_u32_u24_sdwa v1, v34, s57 dst_sel:DWORD dst_unused:UNUSED_PAD src0_sel:WORD_0 src1_sel:DWORD
	v_lshrrev_b32_e32 v1, 21, v1
	v_mul_lo_u16_e32 v35, 36, v1
	v_sub_u16_e32 v35, v34, v35
	v_lshlrev_b32_e32 v124, 2, v35
	v_lshl_add_u64 v[38:39], s[42:43], 0, v[124:125]
	v_lshl_add_u64 v[36:37], s[38:39], 0, v[124:125]
	v_lshl_add_u64 v[38:39], v[38:39], 0, -16
	v_cmp_gt_u16_e32 vcc, 4, v35
	s_nop 1
	v_cndmask_b32_e32 v37, v39, v37, vcc
	v_cndmask_b32_e32 v36, v38, v36, vcc
	v_lshlrev_b32_e32 v35, 2, v34
	v_add_u32_e32 v35, 0x26c00, v35
	ds_read_b32 v35, v35
	v_mul_u32_u24_e32 v37, 0xc0, v1
	v_add_u32_e32 v36, 0x200, v34
	v_add3_u32 v42, s3, v124, v37
	v_cmp_lt_u32_e32 vcc, 63, v34
	v_mov_b32_e32 v34, v36
	ds_read2st64_b32 v[36:37], v42 offset1:12
	ds_read2st64_b32 v[38:39], v42 offset0:24 offset1:36
	ds_read2st64_b32 v[40:41], v42 offset0:48 offset1:60
	ds_read2st64_b32 v[42:43], v42 offset0:72 offset1:84
	v_mul_u32_u24_e32 v1, 0xa0, v1
	s_or_b64 s[8:9], vcc, s[8:9]
	v_add3_u32 v1, s35, v1, v124
	s_waitcnt lgkmcnt(3)
	v_add_f32_e32 v36, 0, v36
	v_add_f32_e32 v36, v36, v37
	s_waitcnt lgkmcnt(2)
	v_add_f32_e32 v36, v36, v38
	v_add_f32_e32 v36, v36, v39
	s_waitcnt lgkmcnt(1)
	v_add_f32_e32 v36, v36, v40
	v_add_f32_e32 v36, v36, v41
	s_waitcnt lgkmcnt(0)
	v_add_f32_e32 v36, v36, v42
	v_add_f32_e32 v36, v36, v43
	v_add_f32_e32 v35, v36, v35
	ds_write_b32 v1, v35
	s_andn2_b64 exec, exec, s[8:9]
	s_cbranch_execnz .LBB0_594

.LBB0_1294:
	s_cmp_lt_i32 s30, 14
	s_cselect_b64 s[2:3], -1, 0
	s_and_b64 s[40:41], s[2:3], s[0:1]
	s_andn2_b64 vcc, exec, s[40:41]
	s_cbranch_vccnz .LBB0_1318
	s_cmpk_gt_i32 s93, 0xff
	s_cbranch_scc1 .LBB0_1318
	v_and_b32_e32 v7, 63, v0
	v_mov_b32_e32 v125, 0
	v_readlane_b32 s0, v254, 12
	v_lshlrev_b32_e32 v122, 5, v7
	v_mov_b32_e32 v123, v125
	v_readlane_b32 s1, v254, 13
	v_readlane_b32 s14, v254, 26
	v_readlane_b32 s15, v254, 27
	s_mov_b64 s[0:1], 0x2000
	v_readlane_b32 s6, v254, 18
	v_lshl_add_u64 v[2:3], s[14:15], 0, v[122:123]
	s_waitcnt vmcnt(0)
	v_lshl_add_u64 v[34:35], v[2:3], 0, s[0:1]
	s_mov_b64 s[0:1], 0x3000
	v_lshl_add_u64 v[36:37], v[2:3], 0, s[0:1]
	s_mov_b64 s[0:1], 0x3800
	v_lshl_add_u64 v[38:39], v[2:3], 0, s[0:1]
	v_readlane_b32 s0, v254, 0
	v_readlane_b32 s2, v254, 14
	s_andn2_b32 s0, s0, 63
	v_lshrrev_b32_e32 v1, 4, v7
	v_readlane_b32 s6, v254, 8
	v_readlane_b32 s4, v254, 16
	v_or_b32_e32 v4, s0, v1
	s_lshl_b32 s2, s6, 1
	v_mad_i64_i32 v[4:5], s[0:1], v4, 48, 0
	v_and_b32_e32 v6, 15, v0
	s_mul_i32 s4, s6, 0x4020
	s_or_b32 s33, s2, 1
	v_readlane_b32 s5, v254, 17
	v_or_b32_e32 v4, v4, v6
	s_add_i32 s26, s4, 0
	s_mul_i32 s4, s33, 0x2010
	v_lshl_add_u64 v[40:41], v[4:5], 4, s[28:29]
	s_add_i32 s34, s4, 0
	s_mov_b64 s[4:5], 0x4eb61800
	v_lshl_add_u64 v[132:133], v[40:41], 0, s[4:5]
	s_mov_b64 s[4:5], 0x4eb61900
	v_lshl_add_u64 v[134:135], v[40:41], 0, s[4:5]
	s_mov_b64 s[4:5], 0x4eb61a00
	v_lshl_add_u64 v[136:137], v[40:41], 0, s[4:5]
	s_mov_b64 s[4:5], 0x4eb62400
	v_lshl_add_u64 v[138:139], v[40:41], 0, s[4:5]
	s_mov_b64 s[4:5], 0x4eb62500
	v_lshl_add_u64 v[140:141], v[40:41], 0, s[4:5]
	s_mov_b64 s[4:5], 0x4eb62600
	v_lshl_add_u64 v[142:143], v[40:41], 0, s[4:5]
	s_mov_b64 s[4:5], 0x4eb63000
	v_lshl_add_u64 v[144:145], v[40:41], 0, s[4:5]
	s_mov_b64 s[4:5], 0x4eb63100
	v_lshl_add_u64 v[146:147], v[40:41], 0, s[4:5]
	s_mov_b64 s[4:5], 0x4eb63200
	v_lshl_add_u64 v[148:149], v[40:41], 0, s[4:5]
	s_mov_b64 s[4:5], 0x4eb63c00
	v_lshl_add_u64 v[150:151], v[40:41], 0, s[4:5]
	s_mov_b64 s[4:5], 0x4eb63d00
	v_lshl_add_u64 v[152:153], v[40:41], 0, s[4:5]
	s_mov_b64 s[4:5], 0x4eb63e00
	v_lshl_add_u64 v[154:155], v[40:41], 0, s[4:5]
	s_mov_b64 s[4:5], 0x4eb64800
	v_lshl_add_u64 v[156:157], v[40:41], 0, s[4:5]
	s_mov_b64 s[4:5], 0x4eb64900
	v_lshl_add_u64 v[158:159], v[40:41], 0, s[4:5]
	s_mov_b64 s[4:5], 0x4eb64a00
	v_lshl_add_u64 v[160:161], v[40:41], 0, s[4:5]
	s_mov_b64 s[4:5], 0x4eb65400
	v_lshl_add_u64 v[162:163], v[40:41], 0, s[4:5]
	s_mov_b64 s[4:5], 0x4eb65500
	v_lshl_add_u64 v[164:165], v[40:41], 0, s[4:5]
	s_mov_b64 s[4:5], 0x4eb65600
	v_lshl_add_u64 v[166:167], v[40:41], 0, s[4:5]
	s_mov_b64 s[4:5], 0x4eb66000
	v_lshl_add_u64 v[168:169], v[40:41], 0, s[4:5]
	s_mov_b64 s[4:5], 0x4eb66100
	v_lshl_add_u64 v[170:171], v[40:41], 0, s[4:5]
	s_mov_b64 s[4:5], 0x4eb66200
	v_lshl_add_u64 v[172:173], v[40:41], 0, s[4:5]
	s_mov_b64 s[4:5], 0x4eb66c00
	v_lshl_add_u64 v[174:175], v[40:41], 0, s[4:5]
	s_mov_b64 s[4:5], 0x4eb66d00
	v_lshl_add_u64 v[176:177], v[40:41], 0, s[4:5]
	s_mov_b64 s[4:5], 0x4eb66e00
	s_mov_b64 s[0:1], 0x4eb60000
	v_lshl_add_u64 v[178:179], v[40:41], 0, s[4:5]
	s_mov_b64 s[4:5], 0x4eb67800
	v_readlane_b32 s3, v254, 15
	v_lshl_add_u64 v[126:127], v[40:41], 0, s[0:1]
	s_lshl_b32 s0, s6, 10
	v_lshl_add_u64 v[180:181], v[40:41], 0, s[4:5]
	s_movk_i32 s4, 0x3000
	v_mul_u32_u24_e32 v4, 0x2010, v6
	s_add_i32 s0, s0, 0
	v_and_b32_e32 v5, 48, v7
	s_add_i32 s3, 0, 0x20100
	v_add_co_u32_e32 v42, vcc, s4, v2
	v_lshl_add_u64 v[128:129], s[50:51], 0, v[122:123]
	v_lshlrev_b32_e32 v124, 4, v7
	v_add3_u32 v123, s0, v4, v5
	v_lshl_add_u32 v44, v6, 2, s3
	v_cmp_eq_u32_e64 s[0:1], 0, v7
	v_addc_co_u32_e32 v43, vcc, 0, v3, vcc
	global_load_dwordx4 v[2:5], v[34:35], off offset:16
	global_load_dwordx4 v[6:9], v[34:35], off offset:2048
	global_load_dwordx4 v[10:13], v[34:35], off offset:2064
	global_load_dwordx4 v[14:17], v[36:37], off offset:16
	global_load_dwordx4 v[18:21], v[42:43], off
	global_load_dwordx4 v[22:25], v[42:43], off offset:2048
	global_load_dwordx4 v[26:29], v[42:43], off offset:-4096
	global_load_dwordx4 v[30:33], v[38:39], off offset:16
	s_mov_b64 s[4:5], 0x4eb67900
	v_lshl_add_u64 v[182:183], v[40:41], 0, s[4:5]
	s_mov_b64 s[4:5], 0x4eb67a00
	v_lshl_add_u64 v[184:185], v[40:41], 0, s[4:5]
	s_mov_b64 s[4:5], 0x4eb68400
	v_lshl_add_u64 v[186:187], v[40:41], 0, s[4:5]
	s_mov_b64 s[4:5], 0x4eb68500
	v_lshl_add_u64 v[188:189], v[40:41], 0, s[4:5]
	s_mov_b64 s[4:5], 0x4eb68600
	v_lshl_add_u64 v[190:191], v[40:41], 0, s[4:5]
	s_mov_b64 s[4:5], 0x4eb69000
	v_lshl_add_u64 v[192:193], v[40:41], 0, s[4:5]
	s_mov_b64 s[4:5], 0x4eb69100
	v_lshl_add_u64 v[194:195], v[40:41], 0, s[4:5]
	s_mov_b64 s[4:5], 0x4eb69200
	v_lshl_add_u64 v[196:197], v[40:41], 0, s[4:5]
	s_mov_b64 s[4:5], 0x4eb69c00
	v_lshl_add_u64 v[198:199], v[40:41], 0, s[4:5]
	s_mov_b64 s[4:5], 0x4eb69d00
	v_lshl_add_u64 v[200:201], v[40:41], 0, s[4:5]
	s_mov_b64 s[4:5], 0x4eb69e00
	v_lshl_add_u64 v[202:203], v[40:41], 0, s[4:5]
	s_mov_b64 s[4:5], 0x4eb6a800
	v_lshl_add_u64 v[204:205], v[40:41], 0, s[4:5]
	s_mov_b64 s[4:5], 0x4eb6a900
	v_lshl_add_u64 v[206:207], v[40:41], 0, s[4:5]
	s_mov_b64 s[4:5], 0x4eb6aa00
	v_lshl_add_u64 v[208:209], v[40:41], 0, s[4:5]
	s_mov_b64 s[4:5], 0x4eb6b400
	v_lshl_add_u64 v[210:211], v[40:41], 0, s[4:5]
	s_mov_b64 s[4:5], 0x4eb6b500
	v_lshlrev_b32_e32 v1, 2, v1
	v_lshl_add_u64 v[212:213], v[40:41], 0, s[4:5]
	s_mov_b64 s[4:5], 0x4eb6b600
	v_lshl_or_b32 v1, s6, 4, v1
	v_lshl_add_u64 v[214:215], v[40:41], 0, s[4:5]
	s_movk_i32 s4, 0xc0
	v_mul_lo_u32 v1, v1, s4
	s_mul_i32 s4, s6, 0x140
	s_add_i32 s35, 0, 0x26100
	s_add_i32 s68, s35, s4
	s_mul_i32 s4, s33, 0xa0
	v_readlane_b32 s10, v254, 22
	v_readlane_b32 s11, v254, 23
	s_add_i32 s69, s35, s4
	s_movk_i32 s4, 0x240
	s_add_i32 s6, 0, 0x26b00
	v_mbcnt_lo_u32_b32 v34, -1, 0
	v_lshl_add_u64 v[130:131], s[36:37], 0, v[124:125]
	v_cmp_gt_u32_e64 s[10:11], 32, v0
	v_cmp_gt_u32_e64 s[4:5], s4, v0
	v_lshl_add_u32 v218, v0, 2, s6
	s_mov_b64 s[54:55], 0x1000
	s_movk_i32 s70, 0x1000
	s_mov_b64 s[56:57], 0x1800
	v_mbcnt_hi_u32_b32 v220, -1, v34
	v_mov_b32_e32 v221, 0x358637bd
	s_mov_b32 s71, 0xf800000
	v_mov_b32_e32 v222, 0x260
	v_add_u32_e32 v223, v44, v1
	s_mov_b32 s72, 0xe38f
	s_mov_b64 s[58:59], 0x70
	s_mov_b32 s73, 0xff61b1e6
	v_mov_b32_e32 v224, 0xff61b1e6
	v_readlane_b32 s7, v254, 19
	v_readlane_b32 s8, v254, 20
	v_readlane_b32 s9, v254, 21
	v_readlane_b32 s12, v254, 24
	v_readlane_b32 s13, v254, 25
	v_mov_b32_e32 v40, v0
	v_mov_b32_e32 v45, 0
	v_mul_u32_u24_sdwa v41, v40, s72 dst_sel:DWORD dst_unused:UNUSED_PAD src0_sel:WORD_0 src1_sel:DWORD
	v_lshrrev_b32_e32 v41, 21, v41
	v_mul_lo_u16_e32 v42, 36, v41
	v_sub_u16_e32 v42, v40, v42
	v_lshlrev_b32_e32 v44, 2, v42
	v_lshl_add_u64 v[36:37], s[38:39], 0, v[44:45]
	v_lshl_add_u64 v[38:39], s[42:43], 0, v[44:45]
	v_lshl_add_u64 v[36:37], v[36:37], 0, 16
	v_lshl_add_u64 v[38:39], v[38:39], 0, s[58:59]
	v_cmp_gt_u16_e32 vcc, 4, v42
	s_nop 1
	v_cndmask_b32_e32 v37, v39, v37, vcc
	v_cndmask_b32_e32 v36, v38, v36, vcc
	global_load_dword v42, v[36:37], off
	v_lshlrev_b32_e32 v43, 2, v40
	v_add_u32_e32 v43, 0x26c00, v43
	s_waitcnt vmcnt(0)
	ds_write_b32 v43, v42
	v_add_u32_e32 v40, 0x200, v40
	v_cmp_gt_u32_e32 vcc, 0x240, v40
	s_and_saveexec_b64 s[14:15], vcc
	v_mul_u32_u24_sdwa v41, v40, s72 dst_sel:DWORD dst_unused:UNUSED_PAD src0_sel:WORD_0 src1_sel:DWORD
	v_lshrrev_b32_e32 v41, 21, v41
	v_mul_lo_u16_e32 v42, 36, v41
	v_sub_u16_e32 v42, v40, v42
	v_lshlrev_b32_e32 v44, 2, v42
	v_lshl_add_u64 v[36:37], s[38:39], 0, v[44:45]
	v_lshl_add_u64 v[38:39], s[42:43], 0, v[44:45]
	v_lshl_add_u64 v[36:37], v[36:37], 0, 16
	v_lshl_add_u64 v[38:39], v[38:39], 0, s[58:59]
	v_cmp_gt_u16_e32 vcc, 4, v42
	s_nop 1
	v_cndmask_b32_e32 v37, v39, v37, vcc
	v_cndmask_b32_e32 v36, v38, v36, vcc
	global_load_dword v42, v[36:37], off
	v_lshlrev_b32_e32 v43, 2, v40
	v_add_u32_e32 v43, 0x26c00, v43
	s_waitcnt vmcnt(0)
	ds_write_b32 v43, v42
	s_or_b64 exec, exec, s[14:15]
	s_branch .LBB0_1298

.LBB0_1298:
	s_and_saveexec_b64 s[6:7], s[10:11]
	ds_write_b32 v218, v125
	s_or_b64 exec, exec, s[6:7]
	s_lshl_b32 s75, s93, 6
	s_add_i32 s76, s75, s2
	s_mov_b32 s77, 0
	s_waitcnt lgkmcnt(0)
	s_barrier
	s_mov_b32 s82, 0
	s_lshl_b32 s82, s82, 4
	s_add_i32 s82, s76, s82
	s_ashr_i32 s83, s82, 31
	s_lshl_b64 s[82:83], s[82:83], 13
	v_lshl_add_u64 v[98:99], v[128:129], 0, s[82:83]
	s_add_u32 s82, s82, 0x1000
	s_addc_u32 s83, s83, 0
	global_load_dwordx4 v[118:121], v[98:99], off
	global_load_dwordx4 v[114:117], v[98:99], off offset:16
	global_load_dwordx4 v[110:113], v[98:99], off offset:2048
	global_load_dwordx4 v[106:109], v[98:99], off offset:2064
	v_lshl_add_u64 v[100:101], v[128:129], 0, s[82:83]
	s_add_u32 s82, s82, 0x1000
	s_addc_u32 s83, s83, 0
	global_load_dwordx4 v[58:61], v[100:101], off offset:2064
	global_load_dwordx4 v[90:93], v[100:101], off
	global_load_dwordx4 v[66:69], v[100:101], off offset:16
	global_load_dwordx4 v[62:65], v[100:101], off offset:2048
	v_lshl_add_u64 v[98:99], v[128:129], 0, s[82:83]
	s_nop 0
	global_load_dwordx4 v[54:57], v[98:99], off
	global_load_dwordx4 v[50:53], v[98:99], off offset:16
	s_branch .LBB0_1303

.LBB0_1303:
	s_lshl_b32 s8, s77, 4
	s_add_i32 s6, s76, s8
	s_ashr_i32 s7, s6, 31
	s_lshl_b64 s[12:13], s[6:7], 13
	v_lshl_add_u64 v[34:35], v[128:129], 0, s[12:13]
	v_lshl_add_u64 v[36:37], v[34:35], 0, s[56:57]
	v_add_co_u32_e32 v36, vcc, 0x1000, v34
	v_and_b32_e32 v1, 64, v220
	s_nop 0
	v_addc_co_u32_e32 v37, vcc, 0, v35, vcc
	v_lshl_add_u64 v[34:35], v[34:35], 0, s[54:55]
	v_xor_b32_e32 v34, 1, v220
	v_add_u32_e32 v1, 64, v1
	s_or_b32 s6, s6, 1
	v_cmp_lt_i32_e32 vcc, v34, v1
	s_ashr_i32 s7, s6, 31
	s_lshl_b64 s[6:7], s[6:7], 13
	v_cndmask_b32_e32 v34, v220, v34, vcc
	v_lshlrev_b32_e32 v225, 2, v34
	v_lshl_add_u64 v[34:35], v[128:129], 0, s[6:7]
	global_load_dwordx4 v[42:45], v[34:35], off offset:2064
	global_load_dwordx4 v[46:49], v[34:35], off offset:2048
	v_add_co_u32_e32 v70, vcc, s70, v34
	v_lshl_add_u64 v[36:37], v[34:35], 0, s[54:55]
	s_nop 0
	v_addc_co_u32_e32 v71, vcc, 0, v35, vcc
	v_lshl_add_u64 v[72:73], v[34:35], 0, s[56:57]
	global_load_dwordx4 v[38:41], v[70:71], off
	s_nop 0
	global_load_dwordx4 v[34:37], v[36:37], off offset:16
	s_add_i32 s8, s8, s75
	s_add_i32 s60, s8, s2
	s_ashr_i32 s61, s60, 31
	s_add_i32 s62, s8, s33
	s_ashr_i32 s63, s62, 31
	s_waitcnt vmcnt(13)
	v_mov_b32_e32 v76, v119
	s_waitcnt vmcnt(12)
	v_mov_b32_e32 v77, v115
	v_mov_b32_e32 v80, v121
	v_mov_b32_e32 v81, v117
	v_mov_b32_e32 v74, v118
	v_mov_b32_e32 v75, v114
	v_mov_b32_e32 v78, v120
	v_mov_b32_e32 v79, v116
	s_waitcnt vmcnt(11)
	v_pk_mul_f32 v[82:83], v[112:113], v[112:113]
	v_pk_mul_f32 v[84:85], v[110:111], v[110:111]
	v_pk_mul_f32 v[76:77], v[76:77], v[76:77]
	v_pk_mul_f32 v[80:81], v[80:81], v[80:81]
	v_pk_mov_b32 v[94:95], v[84:85], v[82:83] op_sel:[1,0]
	v_mov_b32_e32 v85, v83
	v_pk_fma_f32 v[74:75], v[74:75], v[74:75], v[76:77]
	v_pk_fma_f32 v[76:77], v[78:79], v[78:79], v[80:81]
	s_waitcnt vmcnt(10)
	v_mul_f32_e32 v86, v107, v107
	v_mul_f32_e32 v88, v109, v109
	v_pk_add_f32 v[78:79], v[94:95], v[84:85]
	v_pk_add_f32 v[74:75], v[74:75], v[76:77]
	v_pk_fma_f32 v[82:83], v[106:107], v[106:107], v[86:87] op_sel_hi:[1,1,0]
	v_pk_fma_f32 v[86:87], v[108:109], v[108:109], v[88:89] op_sel_hi:[1,1,0]
	s_waitcnt vmcnt(8)
	v_mul_f32_e32 v95, v90, v90
	v_mul_f32_e32 v100, v91, v91
	v_pk_add_f32 v[76:77], v[78:79], v[78:79] op_sel:[0,1] op_sel_hi:[1,0]
	v_pk_add_f32 v[74:75], v[74:75], v[74:75] op_sel:[0,1] op_sel_hi:[1,0]
	v_mul_f32_e32 v83, v92, v92
	v_mul_f32_e32 v87, v93, v93
	s_waitcnt vmcnt(7)
	v_pk_mul_f32 v[80:81], v[68:69], v[68:69]
	v_pk_mul_f32 v[84:85], v[66:67], v[66:67]
	v_mov_b32_e32 v77, v100
	v_mov_b32_e32 v75, v95
	v_pk_mov_b32 v[78:79], v[84:85], v[80:81] op_sel:[1,0]
	v_mov_b32_e32 v85, v81
	v_pk_add_f32 v[82:83], v[82:83], v[86:87]
	v_pk_add_f32 v[74:75], v[74:75], v[76:77]
	s_waitcnt vmcnt(6)
	v_mul_f32_e32 v88, v63, v63
	v_mul_f32_e32 v94, v65, v65
	v_pk_add_f32 v[78:79], v[78:79], v[84:85]
	v_pk_add_f32 v[74:75], v[74:75], v[82:83]
	v_mul_f32_e32 v96, v58, v58
	v_mul_f32_e32 v97, v59, v59
	v_mul_f32_e32 v98, v60, v60
	v_mul_f32_e32 v99, v61, v61
	v_pk_fma_f32 v[80:81], v[62:63], v[62:63], v[88:89] op_sel_hi:[1,1,0]
	v_pk_fma_f32 v[88:89], v[64:65], v[64:65], v[94:95] op_sel_hi:[1,1,0]
	v_pk_add_f32 v[78:79], v[78:79], v[78:79] op_sel:[0,1] op_sel_hi:[1,0]
	v_pk_add_f32 v[74:75], v[74:75], v[74:75] op_sel:[0,1] op_sel_hi:[1,0]
	v_mov_b32_e32 v81, v98
	v_mov_b32_e32 v79, v97
	v_mov_b32_e32 v75, v96
	v_mov_b32_e32 v89, v99
	v_pk_add_f32 v[74:75], v[74:75], v[78:79]
	v_pk_add_f32 v[76:77], v[80:81], v[88:89]
	global_load_dwordx4 v[102:105], v[70:71], off offset:2048
	global_load_dwordx4 v[98:101], v[72:73], off offset:16
	global_load_dwordx4 v[82:85], v[126:127], off
	global_load_dwordx4 v[86:89], v[126:127], off offset:256
	v_pk_add_f32 v[74:75], v[74:75], v[76:77]
	v_xor_b32_e32 v76, 2, v220
	v_add_f32_e32 v74, v74, v75
	ds_bpermute_b32 v75, v225, v74
	v_cmp_lt_i32_e32 vcc, v76, v1
	s_waitcnt lgkmcnt(0)
	v_add_f32_e32 v74, v74, v75
	v_cndmask_b32_e32 v76, v220, v76, vcc
	v_lshlrev_b32_e32 v230, 2, v76
	ds_bpermute_b32 v75, v230, v74
	v_xor_b32_e32 v76, 4, v220
	v_cmp_lt_i32_e32 vcc, v76, v1
	s_waitcnt lgkmcnt(0)
	v_add_f32_e32 v74, v74, v75
	v_cndmask_b32_e32 v76, v220, v76, vcc
	v_lshlrev_b32_e32 v231, 2, v76
	ds_bpermute_b32 v75, v231, v74
	v_xor_b32_e32 v76, 8, v220
	v_cmp_lt_i32_e32 vcc, v76, v1
	s_waitcnt lgkmcnt(0)
	v_add_f32_e32 v74, v74, v75
	v_cndmask_b32_e32 v76, v220, v76, vcc
	v_lshlrev_b32_e32 v232, 2, v76
	ds_bpermute_b32 v75, v232, v74
	v_xor_b32_e32 v76, 16, v220
	v_cmp_lt_i32_e32 vcc, v76, v1
	s_waitcnt lgkmcnt(0)
	v_add_f32_e32 v74, v74, v75
	v_cndmask_b32_e32 v76, v220, v76, vcc
	v_lshlrev_b32_e32 v233, 2, v76
	ds_bpermute_b32 v75, v233, v74
	v_xor_b32_e32 v76, 32, v220
	v_cmp_lt_i32_e32 vcc, v76, v1
	s_waitcnt lgkmcnt(0)
	v_add_f32_e32 v74, v74, v75
	v_cndmask_b32_e32 v1, v220, v76, vcc
	v_lshlrev_b32_e32 v1, 2, v1
	ds_bpermute_b32 v75, v1, v74
	s_waitcnt lgkmcnt(0)
	v_add_f32_e32 v70, v74, v75
	v_fmamk_f32 v70, v70, 0x3a000000, v221
	v_mul_f32_e32 v71, 0x4f800000, v70
	v_cmp_gt_f32_e32 vcc, s71, v70
	s_nop 1
	v_cndmask_b32_e32 v124, v70, v71, vcc
	v_sqrt_f32_e32 v216, v124
	global_load_dwordx4 v[94:97], v[126:127], off offset:512
	global_load_dwordx4 v[70:73], v[126:127], off offset:3072
	global_load_dwordx4 v[74:77], v[126:127], off offset:3328
	global_load_dwordx4 v[78:81], v[126:127], off offset:3584
	v_add_u32_e32 v217, -1, v216
	v_fma_f32 v226, -v217, v216, v124
	v_cmp_ge_f32_e64 s[6:7], 0, v226
	v_add_u32_e32 v226, 1, v216
	s_nop 0
	v_cndmask_b32_e64 v217, v216, v217, s[6:7]
	v_fma_f32 v216, -v226, v216, v124
	v_cmp_lt_f32_e64 s[6:7], 0, v216
	s_nop 1
	v_cndmask_b32_e64 v216, v217, v226, s[6:7]
	v_mul_f32_e32 v217, 0x37800000, v216
	v_cndmask_b32_e32 v216, v216, v217, vcc
	v_cmp_class_f32_e32 vcc, v124, v222
	s_nop 1
	v_cndmask_b32_e32 v124, v216, v124, vcc
	v_div_scale_f32 v216, s[6:7], v124, v124, 1.0
	v_rcp_f32_e32 v217, v216
	s_lshl_b64 s[6:7], s[60:61], 12
	v_fma_f32 v226, -v216, v217, 1.0
	v_fmac_f32_e32 v217, v226, v217
	v_div_scale_f32 v226, vcc, 1.0, v124, 1.0
	v_mul_f32_e32 v227, v226, v217
	v_fma_f32 v228, -v216, v227, v226
	v_fmac_f32_e32 v227, v228, v217
	v_fma_f32 v216, -v216, v227, v226
	v_div_fmas_f32 v216, v216, v217, v227
	v_div_fixup_f32 v124, v216, v124, 1.0
	v_pk_mul_f32 v[118:119], v[118:119], v[124:125] op_sel_hi:[1,0]
	v_pk_mul_f32 v[120:121], v[120:121], v[124:125] op_sel_hi:[1,0]
	v_pk_mul_f32 v[114:115], v[114:115], v[124:125] op_sel_hi:[1,0]
	v_pk_mul_f32 v[116:117], v[116:117], v[124:125] op_sel_hi:[1,0]
	v_pk_mul_f32 v[120:121], v[28:29], v[120:121]
	v_pk_mul_f32 v[118:119], v[26:27], v[118:119]
	v_pk_mul_f32 v[116:117], v[4:5], v[116:117]
	v_pk_mul_f32 v[114:115], v[2:3], v[114:115]
	v_lshl_add_u64 v[216:217], v[130:131], 0, s[6:7]
	v_cvt_pk_bf16_f32 v226, v118, v119
	v_cvt_pk_bf16_f32 v227, v120, v121
	v_cvt_pk_bf16_f32 v228, v114, v115
	v_cvt_pk_bf16_f32 v229, v116, v117
	v_pk_mul_f32 v[110:111], v[110:111], v[124:125] op_sel_hi:[1,0]
	v_pk_mul_f32 v[112:113], v[112:113], v[124:125] op_sel_hi:[1,0]
	v_pk_mul_f32 v[106:107], v[106:107], v[124:125] op_sel_hi:[1,0]
	v_pk_mul_f32 v[108:109], v[108:109], v[124:125] op_sel_hi:[1,0]
	global_store_dwordx4 v[216:217], v[226:229], off
	v_pk_mul_f32 v[112:113], v[8:9], v[112:113]
	v_pk_mul_f32 v[110:111], v[6:7], v[110:111]
	v_add_u32_e32 v226, s26, v122
	v_pk_mul_f32 v[108:109], v[12:13], v[108:109]
	v_pk_mul_f32 v[106:107], v[10:11], v[106:107]
	ds_write_b128 v226, v[118:121]
	ds_write_b128 v226, v[114:117] offset:16
	v_cvt_pk_bf16_f32 v114, v110, v111
	v_cvt_pk_bf16_f32 v115, v112, v113
	v_cvt_pk_bf16_f32 v116, v106, v107
	v_cvt_pk_bf16_f32 v117, v108, v109
	global_store_dwordx4 v[216:217], v[114:117], off offset:1024
	ds_write_b128 v226, v[110:113] offset:2048
	ds_write_b128 v226, v[106:109] offset:2064
	s_waitcnt vmcnt(15)
	v_mov_b32_e32 v108, v55
	s_waitcnt vmcnt(14)
	v_mov_b32_e32 v109, v51
	v_mov_b32_e32 v106, v54
	v_mov_b32_e32 v107, v50
	v_pk_mul_f32 v[108:109], v[108:109], v[108:109]
	v_mov_b32_e32 v110, v57
	v_mov_b32_e32 v111, v53
	v_pk_fma_f32 v[106:107], v[106:107], v[106:107], v[108:109]
	v_mov_b32_e32 v108, v56
	v_mov_b32_e32 v109, v52
	v_pk_mul_f32 v[110:111], v[110:111], v[110:111]
	v_pk_mul_f32 v[90:91], v[90:91], v[124:125] op_sel_hi:[1,0]
	v_pk_fma_f32 v[108:109], v[108:109], v[108:109], v[110:111]
	s_waitcnt vmcnt(12)
	v_pk_mul_f32 v[110:111], v[46:47], v[46:47]
	v_pk_add_f32 v[106:107], v[106:107], v[108:109]
	v_pk_mul_f32 v[108:109], v[48:49], v[48:49]
	v_pk_add_f32 v[106:107], v[106:107], v[106:107] op_sel:[0,1] op_sel_hi:[1,0]
	v_pk_mov_b32 v[112:113], v[110:111], v[108:109] op_sel:[1,0]
	v_mov_b32_e32 v111, v109
	v_pk_add_f32 v[108:109], v[112:113], v[110:111]
	s_waitcnt vmcnt(11)
	v_mul_f32_e32 v110, v38, v38
	v_mul_f32_e32 v111, v39, v39
	v_pk_add_f32 v[108:109], v[108:109], v[108:109] op_sel:[0,1] op_sel_hi:[1,0]
	v_mov_b32_e32 v107, v110
	v_mov_b32_e32 v109, v111
	v_pk_add_f32 v[106:107], v[106:107], v[108:109]
	v_mul_f32_e32 v108, v43, v43
	v_mul_f32_e32 v110, v45, v45
	v_mul_f32_e32 v112, v40, v40
	v_mul_f32_e32 v113, v41, v41
	v_pk_fma_f32 v[108:109], v[42:43], v[42:43], v[108:109] op_sel_hi:[1,1,0]
	v_pk_fma_f32 v[110:111], v[44:45], v[44:45], v[110:111] op_sel_hi:[1,1,0]
	v_mov_b32_e32 v109, v112
	v_mov_b32_e32 v111, v113
	v_pk_add_f32 v[108:109], v[108:109], v[110:111]
	s_waitcnt vmcnt(10)
	v_pk_mul_f32 v[110:111], v[34:35], v[34:35]
	v_pk_add_f32 v[106:107], v[106:107], v[108:109]
	v_pk_mul_f32 v[108:109], v[36:37], v[36:37]
	v_pk_add_f32 v[106:107], v[106:107], v[106:107] op_sel:[0,1] op_sel_hi:[1,0]
	v_pk_mov_b32 v[112:113], v[110:111], v[108:109] op_sel:[1,0]
	v_mov_b32_e32 v111, v109
	v_pk_add_f32 v[108:109], v[112:113], v[110:111]
	s_waitcnt vmcnt(8)
	v_mul_f32_e32 v110, v98, v98
	v_mul_f32_e32 v111, v99, v99
	v_pk_add_f32 v[108:109], v[108:109], v[108:109] op_sel:[0,1] op_sel_hi:[1,0]
	v_mov_b32_e32 v107, v110
	v_mov_b32_e32 v109, v111
	v_pk_add_f32 v[106:107], v[106:107], v[108:109]
	v_mul_f32_e32 v108, v103, v103
	v_mul_f32_e32 v110, v105, v105
	v_mul_f32_e32 v112, v100, v100
	v_mul_f32_e32 v113, v101, v101
	v_pk_fma_f32 v[108:109], v[102:103], v[102:103], v[108:109] op_sel_hi:[1,1,0]
	v_pk_fma_f32 v[110:111], v[104:105], v[104:105], v[110:111] op_sel_hi:[1,1,0]
	v_mov_b32_e32 v109, v112
	v_mov_b32_e32 v111, v113
	v_pk_add_f32 v[108:109], v[108:109], v[110:111]
	v_pk_mul_f32 v[92:93], v[92:93], v[124:125] op_sel_hi:[1,0]
	v_pk_add_f32 v[106:107], v[106:107], v[108:109]
	v_pk_mul_f32 v[66:67], v[66:67], v[124:125] op_sel_hi:[1,0]
	v_add_f32_e32 v106, v106, v107
	ds_bpermute_b32 v107, v225, v106
	v_pk_mul_f32 v[68:69], v[68:69], v[124:125] op_sel_hi:[1,0]
	v_pk_mul_f32 v[92:93], v[20:21], v[92:93]
	v_pk_mul_f32 v[90:91], v[18:19], v[90:91]
	v_pk_mul_f32 v[68:69], v[16:17], v[68:69]
	s_waitcnt lgkmcnt(0)
	v_add_f32_e32 v107, v106, v107
	ds_bpermute_b32 v108, v230, v107
	v_pk_mul_f32 v[66:67], v[14:15], v[66:67]
	v_cvt_pk_bf16_f32 v106, v90, v91
	v_cvt_pk_bf16_f32 v109, v68, v69
	v_pk_mul_f32 v[62:63], v[62:63], v[124:125] op_sel_hi:[1,0]
	s_waitcnt lgkmcnt(0)
	v_add_f32_e32 v110, v107, v108
	ds_bpermute_b32 v111, v231, v110
	v_cvt_pk_bf16_f32 v107, v92, v93
	v_cvt_pk_bf16_f32 v108, v66, v67
	global_store_dwordx4 v[216:217], v[106:109], off offset:2048
	ds_write_b128 v226, v[90:93] offset:4096
	ds_write_b128 v226, v[66:69] offset:4112
	s_waitcnt lgkmcnt(2)
	v_add_f32_e32 v106, v110, v111
	ds_bpermute_b32 v107, v232, v106
	v_pk_mul_f32 v[64:65], v[64:65], v[124:125] op_sel_hi:[1,0]
	v_pk_mul_f32 v[58:59], v[58:59], v[124:125] op_sel_hi:[1,0]
	v_pk_mul_f32 v[60:61], v[60:61], v[124:125] op_sel_hi:[1,0]
	v_pk_mul_f32 v[64:65], v[24:25], v[64:65]
	s_waitcnt lgkmcnt(0)
	v_add_f32_e32 v66, v106, v107
	ds_bpermute_b32 v67, v233, v66
	v_pk_mul_f32 v[62:63], v[22:23], v[62:63]
	v_pk_mul_f32 v[60:61], v[32:33], v[60:61]
	v_pk_mul_f32 v[58:59], v[30:31], v[58:59]
	v_cvt_pk_bf16_f32 v69, v60, v61
	s_waitcnt lgkmcnt(0)
	v_add_f32_e32 v68, v66, v67
	ds_bpermute_b32 v1, v1, v68
	v_cvt_pk_bf16_f32 v66, v62, v63
	v_cvt_pk_bf16_f32 v67, v64, v65
	s_waitcnt lgkmcnt(0)
	v_add_f32_e32 v1, v68, v1
	v_fmamk_f32 v1, v1, 0x3a000000, v221
	v_mul_f32_e32 v68, 0x4f800000, v1
	v_cmp_gt_f32_e32 vcc, s71, v1
	s_nop 1
	v_cndmask_b32_e32 v1, v1, v68, vcc
	v_sqrt_f32_e32 v90, v1
	v_cvt_pk_bf16_f32 v68, v58, v59
	global_store_dwordx4 v[216:217], v[66:69], off offset:3072
	ds_write_b128 v226, v[62:65] offset:6144
	ds_write_b128 v226, v[58:61] offset:6160
	v_add_u32_e32 v66, -1, v90
	v_fma_f32 v67, -v66, v90, v1
	v_cmp_ge_f32_e64 s[6:7], 0, v67
	v_add_u32_e32 v67, 1, v90
	v_fma_f32 v68, -v67, v90, v1
	v_cndmask_b32_e64 v66, v90, v66, s[6:7]
	v_cmp_lt_f32_e64 s[6:7], 0, v68
	s_nop 1
	v_cndmask_b32_e64 v66, v66, v67, s[6:7]
	v_mul_f32_e32 v67, 0x37800000, v66
	v_cndmask_b32_e32 v66, v66, v67, vcc
	v_cmp_class_f32_e32 vcc, v1, v222
	s_nop 1
	v_cndmask_b32_e32 v1, v66, v1, vcc
	v_div_scale_f32 v66, s[6:7], v1, v1, 1.0
	v_rcp_f32_e32 v67, v66
	s_lshl_b64 s[6:7], s[62:63], 12
	v_lshl_add_u64 v[64:65], v[130:131], 0, s[6:7]
	v_fma_f32 v58, -v66, v67, 1.0
	v_fmac_f32_e32 v67, v58, v67
	v_div_scale_f32 v58, vcc, 1.0, v1, 1.0
	v_mul_f32_e32 v59, v58, v67
	v_fma_f32 v60, -v66, v59, v58
	v_fmac_f32_e32 v59, v60, v67
	v_fma_f32 v58, -v66, v59, v58
	v_div_fmas_f32 v58, v58, v67, v59
	v_div_fixup_f32 v62, v58, v1, 1.0
	v_pk_mul_f32 v[54:55], v[54:55], v[62:63] op_sel_hi:[1,0]
	v_pk_mul_f32 v[56:57], v[56:57], v[62:63] op_sel_hi:[1,0]
	v_pk_mul_f32 v[50:51], v[50:51], v[62:63] op_sel_hi:[1,0]
	v_pk_mul_f32 v[52:53], v[52:53], v[62:63] op_sel_hi:[1,0]
	v_pk_mul_f32 v[56:57], v[28:29], v[56:57]
	v_pk_mul_f32 v[54:55], v[26:27], v[54:55]
	v_pk_mul_f32 v[52:53], v[4:5], v[52:53]
	v_pk_mul_f32 v[50:51], v[2:3], v[50:51]
	v_pk_mul_f32 v[46:47], v[46:47], v[62:63] op_sel_hi:[1,0]
	v_pk_mul_f32 v[48:49], v[48:49], v[62:63] op_sel_hi:[1,0]
	v_pk_mul_f32 v[42:43], v[42:43], v[62:63] op_sel_hi:[1,0]
	v_pk_mul_f32 v[44:45], v[44:45], v[62:63] op_sel_hi:[1,0]
	v_cvt_pk_bf16_f32 v58, v54, v55
	v_cvt_pk_bf16_f32 v59, v56, v57
	v_cvt_pk_bf16_f32 v60, v50, v51
	v_cvt_pk_bf16_f32 v61, v52, v53
	v_add_u32_e32 v1, s34, v122
	v_pk_mul_f32 v[48:49], v[8:9], v[48:49]
	v_pk_mul_f32 v[46:47], v[6:7], v[46:47]
	v_pk_mul_f32 v[44:45], v[12:13], v[44:45]
	v_pk_mul_f32 v[42:43], v[10:11], v[42:43]
	v_pk_mul_f32 v[38:39], v[38:39], v[62:63] op_sel_hi:[1,0]
	v_pk_mul_f32 v[40:41], v[40:41], v[62:63] op_sel_hi:[1,0]
	v_pk_mul_f32 v[34:35], v[34:35], v[62:63] op_sel_hi:[1,0]
	v_pk_mul_f32 v[36:37], v[36:37], v[62:63] op_sel_hi:[1,0]
	global_store_dwordx4 v[64:65], v[58:61], off
	ds_write_b128 v1, v[54:57]
	ds_write_b128 v1, v[50:53] offset:16
	v_cvt_pk_bf16_f32 v50, v46, v47
	v_cvt_pk_bf16_f32 v51, v48, v49
	v_cvt_pk_bf16_f32 v52, v42, v43
	v_cvt_pk_bf16_f32 v53, v44, v45
	v_pk_mul_f32 v[40:41], v[20:21], v[40:41]
	v_pk_mul_f32 v[38:39], v[18:19], v[38:39]
	v_pk_mul_f32 v[36:37], v[16:17], v[36:37]
	v_pk_mul_f32 v[34:35], v[14:15], v[34:35]
	global_store_dwordx4 v[64:65], v[50:53], off offset:1024
	ds_write_b128 v1, v[46:49] offset:2048
	ds_write_b128 v1, v[42:45] offset:2064
	v_cvt_pk_bf16_f32 v42, v38, v39
	v_cvt_pk_bf16_f32 v43, v40, v41
	v_cvt_pk_bf16_f32 v44, v34, v35
	v_cvt_pk_bf16_f32 v45, v36, v37
	global_store_dwordx4 v[64:65], v[42:45], off offset:2048
	ds_write_b128 v1, v[38:41] offset:4096
	ds_write_b128 v1, v[34:37] offset:4112
	v_pk_mul_f32 v[34:35], v[102:103], v[62:63] op_sel_hi:[1,0]
	v_pk_mul_f32 v[36:37], v[104:105], v[62:63] op_sel_hi:[1,0]
	v_pk_mul_f32 v[38:39], v[98:99], v[62:63] op_sel_hi:[1,0]
	v_pk_mul_f32 v[40:41], v[100:101], v[62:63] op_sel_hi:[1,0]
	v_pk_mul_f32 v[36:37], v[24:25], v[36:37]
	v_pk_mul_f32 v[34:35], v[22:23], v[34:35]
	v_pk_mul_f32 v[40:41], v[32:33], v[40:41]
	v_pk_mul_f32 v[38:39], v[30:31], v[38:39]
	v_cvt_pk_bf16_f32 v42, v34, v35
	v_cvt_pk_bf16_f32 v43, v36, v37
	v_cvt_pk_bf16_f32 v44, v38, v39
	v_cvt_pk_bf16_f32 v45, v40, v41
	global_store_dwordx4 v[64:65], v[42:45], off offset:3072
	ds_write_b128 v1, v[34:37] offset:6144
	ds_write_b128 v1, v[38:41] offset:6160
	s_waitcnt lgkmcnt(0)
	s_barrier
	global_load_dwordx4 v[34:37], v[132:133], off
	global_load_dwordx4 v[38:41], v[134:135], off
	global_load_dwordx4 v[42:45], v[136:137], off
	global_load_dwordx4 v[46:49], v[138:139], off
	global_load_dwordx4 v[50:53], v[140:141], off
	global_load_dwordx4 v[54:57], v[142:143], off
	global_load_dwordx4 v[58:61], v[144:145], off
	global_load_dwordx4 v[62:65], v[146:147], off
	global_load_dwordx4 v[66:69], v[148:149], off
	global_load_dwordx4 v[90:93], v[150:151], off
	global_load_dwordx4 v[98:101], v[152:153], off
	global_load_dwordx4 v[102:105], v[154:155], off
	global_load_dwordx4 v[106:109], v[156:157], off
	global_load_dwordx4 v[110:113], v[158:159], off
	global_load_dwordx4 v[114:117], v[160:161], off
	global_load_dwordx4 v[118:121], v[162:163], off
	global_load_dwordx4 v[226:229], v[164:165], off
	global_load_dwordx4 v[230:233], v[166:167], off
	ds_read_b128 v[234:237], v123
	ds_read_b128 v[238:241], v123 offset:64
	s_waitcnt vmcnt(31) lgkmcnt(1)
	v_mfma_f32_16x16x4_f32 v[242:245], v234, v82, 0
	s_waitcnt vmcnt(30)
	v_mfma_f32_16x16x4_f32 v[246:249], v234, v86, 0
	s_waitcnt vmcnt(29)
	v_mfma_f32_16x16x4_f32 v[250:253], v234, v94, 0
	v_mfma_f32_16x16x4_f32 v[242:245], v235, v83, v[242:245]
	v_mfma_f32_16x16x4_f32 v[246:249], v235, v87, v[246:249]
	v_mfma_f32_16x16x4_f32 v[250:253], v235, v95, v[250:253]
	v_mfma_f32_16x16x4_f32 v[242:245], v236, v84, v[242:245]
	v_mfma_f32_16x16x4_f32 v[246:249], v236, v88, v[246:249]
	v_mfma_f32_16x16x4_f32 v[250:253], v236, v96, v[250:253]
	v_mfma_f32_16x16x4_f32 v[82:85], v237, v85, v[242:245]
	v_mfma_f32_16x16x4_f32 v[86:89], v237, v89, v[246:249]
	v_mfma_f32_16x16x4_f32 v[94:97], v237, v97, v[250:253]
	s_waitcnt vmcnt(28) lgkmcnt(0)
	v_mfma_f32_16x16x4_f32 v[82:85], v238, v70, v[82:85]
	s_waitcnt vmcnt(27)
	v_mfma_f32_16x16x4_f32 v[86:89], v238, v74, v[86:89]
	s_waitcnt vmcnt(26)
	v_mfma_f32_16x16x4_f32 v[94:97], v238, v78, v[94:97]
	v_mfma_f32_16x16x4_f32 v[82:85], v239, v71, v[82:85]
	v_mfma_f32_16x16x4_f32 v[86:89], v239, v75, v[86:89]
	v_mfma_f32_16x16x4_f32 v[94:97], v239, v79, v[94:97]
	v_mfma_f32_16x16x4_f32 v[82:85], v240, v72, v[82:85]
	v_mfma_f32_16x16x4_f32 v[86:89], v240, v76, v[86:89]
	v_mfma_f32_16x16x4_f32 v[94:97], v240, v80, v[94:97]
	v_mfma_f32_16x16x4_f32 v[70:73], v241, v73, v[82:85]
	v_mfma_f32_16x16x4_f32 v[74:77], v241, v77, v[86:89]
	s_nop 5
	ds_read_b128 v[82:85], v123 offset:128
	ds_read_b128 v[86:89], v123 offset:192
	v_mfma_f32_16x16x4_f32 v[78:81], v241, v81, v[94:97]
	s_waitcnt vmcnt(17) lgkmcnt(1)
	v_mfma_f32_16x16x4_f32 v[70:73], v82, v34, v[70:73]
	s_waitcnt vmcnt(16)
	v_mfma_f32_16x16x4_f32 v[74:77], v82, v38, v[74:77]
	s_waitcnt vmcnt(15)
	v_mfma_f32_16x16x4_f32 v[78:81], v82, v42, v[78:81]
	v_mfma_f32_16x16x4_f32 v[70:73], v83, v35, v[70:73]
	v_mfma_f32_16x16x4_f32 v[74:77], v83, v39, v[74:77]
	v_mfma_f32_16x16x4_f32 v[78:81], v83, v43, v[78:81]
	v_mfma_f32_16x16x4_f32 v[70:73], v84, v36, v[70:73]
	v_mfma_f32_16x16x4_f32 v[74:77], v84, v40, v[74:77]
	v_mfma_f32_16x16x4_f32 v[78:81], v84, v44, v[78:81]
	v_mfma_f32_16x16x4_f32 v[34:37], v85, v37, v[70:73]
	v_mfma_f32_16x16x4_f32 v[38:41], v85, v41, v[74:77]
	v_mfma_f32_16x16x4_f32 v[42:45], v85, v45, v[78:81]
	s_waitcnt vmcnt(12) lgkmcnt(0)
	v_mfma_f32_16x16x4_f32 v[42:45], v86, v54, v[42:45]
	v_mfma_f32_16x16x4_f32 v[34:37], v86, v46, v[34:37]
	v_mfma_f32_16x16x4_f32 v[38:41], v86, v50, v[38:41]
	v_mfma_f32_16x16x4_f32 v[42:45], v87, v55, v[42:45]
	v_mfma_f32_16x16x4_f32 v[34:37], v87, v47, v[34:37]
	v_mfma_f32_16x16x4_f32 v[38:41], v87, v51, v[38:41]
	v_mfma_f32_16x16x4_f32 v[42:45], v88, v56, v[42:45]
	v_mfma_f32_16x16x4_f32 v[34:37], v88, v48, v[34:37]
	v_mfma_f32_16x16x4_f32 v[38:41], v88, v52, v[38:41]
	v_mfma_f32_16x16x4_f32 v[34:37], v89, v49, v[34:37]
	global_load_dwordx4 v[46:49], v[168:169], off
	global_load_dwordx4 v[70:73], v[170:171], off
	global_load_dwordx4 v[74:77], v[172:173], off
	global_load_dwordx4 v[78:81], v[174:175], off
	v_mfma_f32_16x16x4_f32 v[38:41], v89, v53, v[38:41]
	global_load_dwordx4 v[50:53], v[176:177], off
	global_load_dwordx4 v[82:85], v[178:179], off
	global_load_dwordx4 v[94:97], v[180:181], off
	global_load_dwordx4 v[234:237], v[182:183], off
	global_load_dwordx4 v[238:241], v[184:185], off
	global_load_dwordx4 v[242:245], v[186:187], off
	global_load_dwordx4 v[246:249], v[188:189], off
	global_load_dwordx4 v[250:253], v[190:191], off
	v_mfma_f32_16x16x4_f32 v[42:45], v89, v57, v[42:45]
	ds_read_b128 v[54:57], v123 offset:256
	ds_read_b128 v[86:89], v123 offset:320
	s_waitcnt vmcnt(23) lgkmcnt(1)
	v_mfma_f32_16x16x4_f32 v[34:37], v54, v58, v[34:37]
	s_waitcnt vmcnt(22)
	v_mfma_f32_16x16x4_f32 v[38:41], v54, v62, v[38:41]
	s_waitcnt vmcnt(21)
	v_mfma_f32_16x16x4_f32 v[42:45], v54, v66, v[42:45]
	v_mfma_f32_16x16x4_f32 v[34:37], v55, v59, v[34:37]
	v_mfma_f32_16x16x4_f32 v[38:41], v55, v63, v[38:41]
	v_mfma_f32_16x16x4_f32 v[42:45], v55, v67, v[42:45]
	v_mfma_f32_16x16x4_f32 v[34:37], v56, v60, v[34:37]
	v_mfma_f32_16x16x4_f32 v[38:41], v56, v64, v[38:41]
	v_mfma_f32_16x16x4_f32 v[42:45], v56, v68, v[42:45]
	v_mfma_f32_16x16x4_f32 v[34:37], v57, v61, v[34:37]
	v_mfma_f32_16x16x4_f32 v[38:41], v57, v65, v[38:41]
	v_mfma_f32_16x16x4_f32 v[42:45], v57, v69, v[42:45]
	ds_read_b128 v[54:57], v123 offset:384
	ds_read_b128 v[58:61], v123 offset:448
	s_waitcnt vmcnt(20) lgkmcnt(2)
	v_mfma_f32_16x16x4_f32 v[34:37], v86, v90, v[34:37]
	s_waitcnt vmcnt(19)
	v_mfma_f32_16x16x4_f32 v[38:41], v86, v98, v[38:41]
	s_waitcnt vmcnt(18)
	v_mfma_f32_16x16x4_f32 v[42:45], v86, v102, v[42:45]
	v_mfma_f32_16x16x4_f32 v[34:37], v87, v91, v[34:37]
	v_mfma_f32_16x16x4_f32 v[38:41], v87, v99, v[38:41]
	v_mfma_f32_16x16x4_f32 v[42:45], v87, v103, v[42:45]
	v_mfma_f32_16x16x4_f32 v[34:37], v88, v92, v[34:37]
	v_mfma_f32_16x16x4_f32 v[38:41], v88, v100, v[38:41]
	v_mfma_f32_16x16x4_f32 v[42:45], v88, v104, v[42:45]
	v_mfma_f32_16x16x4_f32 v[34:37], v89, v93, v[34:37]
	v_mfma_f32_16x16x4_f32 v[38:41], v89, v101, v[38:41]
	v_mfma_f32_16x16x4_f32 v[42:45], v89, v105, v[42:45]
	s_waitcnt vmcnt(17) lgkmcnt(1)
	v_mfma_f32_16x16x4_f32 v[34:37], v54, v106, v[34:37]
	s_waitcnt vmcnt(16)
	v_mfma_f32_16x16x4_f32 v[38:41], v54, v110, v[38:41]
	s_waitcnt vmcnt(15)
	v_mfma_f32_16x16x4_f32 v[42:45], v54, v114, v[42:45]
	v_mfma_f32_16x16x4_f32 v[34:37], v55, v107, v[34:37]
	v_mfma_f32_16x16x4_f32 v[38:41], v55, v111, v[38:41]
	v_mfma_f32_16x16x4_f32 v[42:45], v55, v115, v[42:45]
	v_mfma_f32_16x16x4_f32 v[34:37], v56, v108, v[34:37]
	v_mfma_f32_16x16x4_f32 v[38:41], v56, v112, v[38:41]
	v_mfma_f32_16x16x4_f32 v[42:45], v56, v116, v[42:45]
	v_mfma_f32_16x16x4_f32 v[34:37], v57, v109, v[34:37]
	v_mfma_f32_16x16x4_f32 v[38:41], v57, v113, v[38:41]
	v_mfma_f32_16x16x4_f32 v[42:45], v57, v117, v[42:45]
	global_load_dwordx4 v[54:57], v[192:193], off
	global_load_dwordx4 v[62:65], v[194:195], off
	global_load_dwordx4 v[66:69], v[196:197], off
	global_load_dwordx4 v[86:89], v[198:199], off
	s_waitcnt vmcnt(16) lgkmcnt(0)
	v_mfma_f32_16x16x4_f32 v[42:45], v58, v230, v[42:45]
	v_mfma_f32_16x16x4_f32 v[34:37], v58, v118, v[34:37]
	v_mfma_f32_16x16x4_f32 v[38:41], v58, v226, v[38:41]
	v_mfma_f32_16x16x4_f32 v[42:45], v59, v231, v[42:45]
	v_mfma_f32_16x16x4_f32 v[34:37], v59, v119, v[34:37]
	v_mfma_f32_16x16x4_f32 v[38:41], v59, v227, v[38:41]
	v_mfma_f32_16x16x4_f32 v[42:45], v60, v232, v[42:45]
	v_mfma_f32_16x16x4_f32 v[34:37], v60, v120, v[34:37]
	v_mfma_f32_16x16x4_f32 v[38:41], v60, v228, v[38:41]
	v_mfma_f32_16x16x4_f32 v[34:37], v61, v121, v[34:37]
	v_mfma_f32_16x16x4_f32 v[38:41], v61, v229, v[38:41]
	global_load_dwordx4 v[90:93], v[200:201], off
	global_load_dwordx4 v[98:101], v[202:203], off
	global_load_dwordx4 v[102:105], v[204:205], off
	global_load_dwordx4 v[106:109], v[206:207], off
	global_load_dwordx4 v[110:113], v[208:209], off
	global_load_dwordx4 v[114:117], v[210:211], off
	global_load_dwordx4 v[118:121], v[212:213], off
	global_load_dwordx4 v[226:229], v[214:215], off
	v_mfma_f32_16x16x4_f32 v[42:45], v61, v233, v[42:45]
	ds_read_b128 v[58:61], v123 offset:512
	ds_read_b128 v[230:233], v123 offset:576
	s_waitcnt vmcnt(23) lgkmcnt(1)
	v_mfma_f32_16x16x4_f32 v[34:37], v58, v46, v[34:37]
	s_waitcnt vmcnt(22)
	v_mfma_f32_16x16x4_f32 v[38:41], v58, v70, v[38:41]
	s_waitcnt vmcnt(21)
	v_mfma_f32_16x16x4_f32 v[42:45], v58, v74, v[42:45]
	v_mfma_f32_16x16x4_f32 v[34:37], v59, v47, v[34:37]
	v_mfma_f32_16x16x4_f32 v[38:41], v59, v71, v[38:41]
	v_mfma_f32_16x16x4_f32 v[42:45], v59, v75, v[42:45]
	v_mfma_f32_16x16x4_f32 v[34:37], v60, v48, v[34:37]
	v_mfma_f32_16x16x4_f32 v[38:41], v60, v72, v[38:41]
	v_mfma_f32_16x16x4_f32 v[42:45], v60, v76, v[42:45]
	v_mfma_f32_16x16x4_f32 v[34:37], v61, v49, v[34:37]
	v_mfma_f32_16x16x4_f32 v[38:41], v61, v73, v[38:41]
	v_mfma_f32_16x16x4_f32 v[42:45], v61, v77, v[42:45]
	s_waitcnt vmcnt(20) lgkmcnt(0)
	v_mfma_f32_16x16x4_f32 v[34:37], v230, v78, v[34:37]
	s_waitcnt vmcnt(19)
	v_mfma_f32_16x16x4_f32 v[38:41], v230, v50, v[38:41]
	s_waitcnt vmcnt(18)
	v_mfma_f32_16x16x4_f32 v[42:45], v230, v82, v[42:45]
	v_mfma_f32_16x16x4_f32 v[34:37], v231, v79, v[34:37]
	v_mfma_f32_16x16x4_f32 v[38:41], v231, v51, v[38:41]
	v_mfma_f32_16x16x4_f32 v[42:45], v231, v83, v[42:45]
	v_mfma_f32_16x16x4_f32 v[34:37], v232, v80, v[34:37]
	v_mfma_f32_16x16x4_f32 v[38:41], v232, v52, v[38:41]
	v_mfma_f32_16x16x4_f32 v[42:45], v232, v84, v[42:45]
	v_mfma_f32_16x16x4_f32 v[34:37], v233, v81, v[34:37]
	v_mfma_f32_16x16x4_f32 v[38:41], v233, v53, v[38:41]
	ds_read_b128 v[46:49], v123 offset:640
	ds_read_b128 v[50:53], v123 offset:704
	v_mfma_f32_16x16x4_f32 v[42:45], v233, v85, v[42:45]
	s_waitcnt vmcnt(17) lgkmcnt(1)
	v_mfma_f32_16x16x4_f32 v[34:37], v46, v94, v[34:37]
	s_waitcnt vmcnt(16)
	v_mfma_f32_16x16x4_f32 v[38:41], v46, v234, v[38:41]
	s_waitcnt vmcnt(15)
	v_mfma_f32_16x16x4_f32 v[42:45], v46, v238, v[42:45]
	v_mfma_f32_16x16x4_f32 v[34:37], v47, v95, v[34:37]
	v_mfma_f32_16x16x4_f32 v[38:41], v47, v235, v[38:41]
	v_mfma_f32_16x16x4_f32 v[42:45], v47, v239, v[42:45]
	v_mfma_f32_16x16x4_f32 v[34:37], v48, v96, v[34:37]
	v_mfma_f32_16x16x4_f32 v[38:41], v48, v236, v[38:41]
	v_mfma_f32_16x16x4_f32 v[42:45], v48, v240, v[42:45]
	v_mfma_f32_16x16x4_f32 v[34:37], v49, v97, v[34:37]
	v_mfma_f32_16x16x4_f32 v[38:41], v49, v237, v[38:41]
	v_mfma_f32_16x16x4_f32 v[42:45], v49, v241, v[42:45]
	s_waitcnt vmcnt(14) lgkmcnt(0)
	v_mfma_f32_16x16x4_f32 v[34:37], v50, v242, v[34:37]
	s_waitcnt vmcnt(13)
	v_mfma_f32_16x16x4_f32 v[38:41], v50, v246, v[38:41]
	s_waitcnt vmcnt(12)
	v_mfma_f32_16x16x4_f32 v[42:45], v50, v250, v[42:45]
	v_mfma_f32_16x16x4_f32 v[34:37], v51, v243, v[34:37]
	v_mfma_f32_16x16x4_f32 v[38:41], v51, v247, v[38:41]
	v_mfma_f32_16x16x4_f32 v[42:45], v51, v251, v[42:45]
	v_mfma_f32_16x16x4_f32 v[34:37], v52, v244, v[34:37]
	v_mfma_f32_16x16x4_f32 v[38:41], v52, v248, v[38:41]
	v_mfma_f32_16x16x4_f32 v[42:45], v52, v252, v[42:45]
	v_mfma_f32_16x16x4_f32 v[34:37], v53, v245, v[34:37]
	v_mfma_f32_16x16x4_f32 v[38:41], v53, v249, v[38:41]
	v_mfma_f32_16x16x4_f32 v[42:45], v53, v253, v[42:45]
	ds_read_b128 v[46:49], v123 offset:768
	ds_read_b128 v[50:53], v123 offset:832
	s_waitcnt vmcnt(11) lgkmcnt(1)
	v_mfma_f32_16x16x4_f32 v[34:37], v46, v54, v[34:37]
	s_waitcnt vmcnt(10)
	v_mfma_f32_16x16x4_f32 v[38:41], v46, v62, v[38:41]
	s_waitcnt vmcnt(9)
	v_mfma_f32_16x16x4_f32 v[42:45], v46, v66, v[42:45]
	v_mfma_f32_16x16x4_f32 v[34:37], v47, v55, v[34:37]
	v_mfma_f32_16x16x4_f32 v[38:41], v47, v63, v[38:41]
	v_mfma_f32_16x16x4_f32 v[42:45], v47, v67, v[42:45]
	v_mfma_f32_16x16x4_f32 v[34:37], v48, v56, v[34:37]
	v_mfma_f32_16x16x4_f32 v[38:41], v48, v64, v[38:41]
	v_mfma_f32_16x16x4_f32 v[42:45], v48, v68, v[42:45]
	v_mfma_f32_16x16x4_f32 v[34:37], v49, v57, v[34:37]
	v_mfma_f32_16x16x4_f32 v[38:41], v49, v65, v[38:41]
	v_mfma_f32_16x16x4_f32 v[42:45], v49, v69, v[42:45]
	s_waitcnt vmcnt(8) lgkmcnt(0)
	v_mfma_f32_16x16x4_f32 v[34:37], v50, v86, v[34:37]
	s_waitcnt vmcnt(7)
	v_mfma_f32_16x16x4_f32 v[38:41], v50, v90, v[38:41]
	s_waitcnt vmcnt(6)
	v_mfma_f32_16x16x4_f32 v[42:45], v50, v98, v[42:45]
	v_mfma_f32_16x16x4_f32 v[34:37], v51, v87, v[34:37]
	v_mfma_f32_16x16x4_f32 v[38:41], v51, v91, v[38:41]
	v_mfma_f32_16x16x4_f32 v[42:45], v51, v99, v[42:45]
	v_mfma_f32_16x16x4_f32 v[34:37], v52, v88, v[34:37]
	v_mfma_f32_16x16x4_f32 v[38:41], v52, v92, v[38:41]
	v_mfma_f32_16x16x4_f32 v[42:45], v52, v100, v[42:45]
	v_mfma_f32_16x16x4_f32 v[34:37], v53, v89, v[34:37]
	v_mfma_f32_16x16x4_f32 v[38:41], v53, v93, v[38:41]
	v_mfma_f32_16x16x4_f32 v[42:45], v53, v101, v[42:45]
	ds_read_b128 v[46:49], v123 offset:896
	ds_read_b128 v[50:53], v123 offset:960
	s_waitcnt vmcnt(5) lgkmcnt(1)
	v_mfma_f32_16x16x4_f32 v[34:37], v46, v102, v[34:37]
	s_waitcnt vmcnt(4)
	v_mfma_f32_16x16x4_f32 v[38:41], v46, v106, v[38:41]
	s_waitcnt vmcnt(3)
	v_mfma_f32_16x16x4_f32 v[42:45], v46, v110, v[42:45]
	v_mfma_f32_16x16x4_f32 v[34:37], v47, v103, v[34:37]
	v_mfma_f32_16x16x4_f32 v[38:41], v47, v107, v[38:41]
	v_mfma_f32_16x16x4_f32 v[42:45], v47, v111, v[42:45]
	v_mfma_f32_16x16x4_f32 v[34:37], v48, v104, v[34:37]
	v_mfma_f32_16x16x4_f32 v[38:41], v48, v108, v[38:41]
	v_mfma_f32_16x16x4_f32 v[42:45], v48, v112, v[42:45]
	v_mfma_f32_16x16x4_f32 v[34:37], v49, v105, v[34:37]
	v_mfma_f32_16x16x4_f32 v[38:41], v49, v109, v[38:41]
	v_mfma_f32_16x16x4_f32 v[42:45], v49, v113, v[42:45]
	s_waitcnt vmcnt(2) lgkmcnt(0)
	v_mfma_f32_16x16x4_f32 v[34:37], v50, v114, v[34:37]
	s_waitcnt vmcnt(1)
	v_mfma_f32_16x16x4_f32 v[38:41], v50, v118, v[38:41]
	s_waitcnt vmcnt(0)
	v_mfma_f32_16x16x4_f32 v[42:45], v50, v226, v[42:45]
	v_mfma_f32_16x16x4_f32 v[34:37], v51, v115, v[34:37]
	v_mfma_f32_16x16x4_f32 v[38:41], v51, v119, v[38:41]
	v_mfma_f32_16x16x4_f32 v[42:45], v51, v227, v[42:45]
	v_mfma_f32_16x16x4_f32 v[34:37], v52, v116, v[34:37]
	v_mfma_f32_16x16x4_f32 v[38:41], v52, v120, v[38:41]
	v_mfma_f32_16x16x4_f32 v[42:45], v52, v228, v[42:45]
	v_mfma_f32_16x16x4_f32 v[34:37], v53, v117, v[34:37]
	v_mfma_f32_16x16x4_f32 v[38:41], v53, v121, v[38:41]
	v_mfma_f32_16x16x4_f32 v[42:45], v53, v229, v[42:45]
	s_cmp_gt_u32 s77, 2
	s_cbranch_scc1 .Lrpf_b_skip
	s_add_i32 s82, s77, 1
	s_lshl_b32 s82, s82, 4
	s_add_i32 s82, s76, s82
	s_ashr_i32 s83, s82, 31
	s_lshl_b64 s[82:83], s[82:83], 13
	v_lshl_add_u64 v[98:99], v[128:129], 0, s[82:83]
	s_add_u32 s82, s82, 0x1000
	s_addc_u32 s83, s83, 0
	global_load_dwordx4 v[118:121], v[98:99], off
	global_load_dwordx4 v[114:117], v[98:99], off offset:16
	global_load_dwordx4 v[110:113], v[98:99], off offset:2048
	global_load_dwordx4 v[106:109], v[98:99], off offset:2064
	v_lshl_add_u64 v[100:101], v[128:129], 0, s[82:83]
	s_add_u32 s82, s82, 0x1000
	s_addc_u32 s83, s83, 0
	global_load_dwordx4 v[58:61], v[100:101], off offset:2064
	global_load_dwordx4 v[90:93], v[100:101], off
	global_load_dwordx4 v[66:69], v[100:101], off offset:16
	global_load_dwordx4 v[62:65], v[100:101], off offset:2048
	v_lshl_add_u64 v[98:99], v[128:129], 0, s[82:83]
	s_nop 0
	global_load_dwordx4 v[54:57], v[98:99], off
	global_load_dwordx4 v[50:53], v[98:99], off offset:16

.LBB0_1305:
	v_mul_u32_u24_sdwa v1, v34, s72 dst_sel:DWORD dst_unused:UNUSED_PAD src0_sel:WORD_0 src1_sel:DWORD
	v_lshrrev_b32_e32 v1, 21, v1
	v_mul_lo_u16_e32 v35, 36, v1
	v_sub_u16_e32 v35, v34, v35
	v_lshlrev_b32_e32 v124, 2, v35
	v_lshl_add_u64 v[36:37], s[38:39], 0, v[124:125]
	v_lshl_add_u64 v[38:39], s[42:43], 0, v[124:125]
	v_lshl_add_u64 v[36:37], v[36:37], 0, 16
	v_lshl_add_u64 v[38:39], v[38:39], 0, s[58:59]
	v_cmp_gt_u16_e32 vcc, 4, v35
	s_nop 1
	v_cndmask_b32_e32 v37, v39, v37, vcc
	v_cndmask_b32_e32 v36, v38, v36, vcc
	v_lshlrev_b32_e32 v35, 2, v34
	v_add_u32_e32 v35, 0x26c00, v35
	ds_read_b32 v35, v35
	v_mul_u32_u24_e32 v37, 0xc0, v1
	v_add_u32_e32 v36, 0x200, v34
	v_add3_u32 v42, s3, v124, v37
	v_cmp_lt_u32_e32 vcc, 63, v34
	v_mov_b32_e32 v34, v36
	ds_read2st64_b32 v[36:37], v42 offset1:12
	ds_read2st64_b32 v[38:39], v42 offset0:24 offset1:36
	ds_read2st64_b32 v[40:41], v42 offset0:48 offset1:60
	ds_read2st64_b32 v[42:43], v42 offset0:72 offset1:84
	v_mul_u32_u24_e32 v1, 0xa0, v1
	s_or_b64 s[8:9], vcc, s[8:9]
	v_add3_u32 v1, s35, v1, v124
	s_waitcnt lgkmcnt(3)
	v_add_f32_e32 v36, 0, v36
	v_add_f32_e32 v36, v36, v37
	s_waitcnt lgkmcnt(2)
	v_add_f32_e32 v36, v36, v38
	v_add_f32_e32 v36, v36, v39
	s_waitcnt lgkmcnt(1)
	v_add_f32_e32 v36, v36, v40
	v_add_f32_e32 v36, v36, v41
	s_waitcnt lgkmcnt(0)
	v_add_f32_e32 v36, v36, v42
	v_add_f32_e32 v36, v36, v43
	v_add_f32_e32 v35, v36, v35
	ds_write_b32 v1, v35
	s_andn2_b64 exec, exec, s[8:9]
	s_cbranch_execnz .LBB0_1305
